# speedup vs baseline: 1.0217x; 1.0217x over previous
.LBB5_2:
	s_lshl_b32 s3, s3, 7
	s_lshl_b32 s16, s2, 7
	v_lshrrev_b32_e32 v1, 1, v0
	v_mov_b32_e32 v65, 0
	v_and_b32_e32 v82, 15, v0
	v_and_b32_e32 v1, 64, v1
	s_cmp_lt_i32 s18, 32
	v_mov_b32_e32 v64, v65
	v_mov_b32_e32 v63, v65
	v_mov_b32_e32 v62, v65
	v_mov_b32_e32 v61, v65
	v_mov_b32_e32 v60, v65
	v_mov_b32_e32 v59, v65
	v_mov_b32_e32 v58, v65
	v_mov_b32_e32 v57, v65
	v_mov_b32_e32 v56, v65
	v_mov_b32_e32 v55, v65
	v_mov_b32_e32 v54, v65
	v_mov_b32_e32 v53, v65
	v_mov_b32_e32 v52, v65
	v_mov_b32_e32 v51, v65
	v_mov_b32_e32 v50, v65
	v_mov_b32_e32 v49, v65
	v_mov_b32_e32 v48, v65
	v_mov_b32_e32 v47, v65
	v_mov_b32_e32 v46, v65
	v_mov_b32_e32 v45, v65
	v_mov_b32_e32 v44, v65
	v_mov_b32_e32 v43, v65
	v_mov_b32_e32 v42, v65
	v_mov_b32_e32 v41, v65
	v_mov_b32_e32 v40, v65
	v_mov_b32_e32 v39, v65
	v_mov_b32_e32 v38, v65
	v_mov_b32_e32 v37, v65
	v_mov_b32_e32 v36, v65
	v_mov_b32_e32 v35, v65
	v_mov_b32_e32 v34, v65
	v_mov_b32_e32 v33, v65
	v_mov_b32_e32 v32, v65
	v_mov_b32_e32 v31, v65
	v_mov_b32_e32 v30, v65
	v_mov_b32_e32 v29, v65
	v_mov_b32_e32 v28, v65
	v_mov_b32_e32 v27, v65
	v_mov_b32_e32 v26, v65
	v_mov_b32_e32 v25, v65
	v_mov_b32_e32 v24, v65
	v_mov_b32_e32 v23, v65
	v_mov_b32_e32 v22, v65
	v_mov_b32_e32 v21, v65
	v_mov_b32_e32 v20, v65
	v_mov_b32_e32 v19, v65
	v_mov_b32_e32 v18, v65
	v_mov_b32_e32 v17, v65
	v_mov_b32_e32 v16, v65
	v_mov_b32_e32 v15, v65
	v_mov_b32_e32 v14, v65
	v_mov_b32_e32 v13, v65
	v_mov_b32_e32 v12, v65
	v_mov_b32_e32 v11, v65
	v_mov_b32_e32 v10, v65
	v_mov_b32_e32 v9, v65
	v_mov_b32_e32 v8, v65
	v_mov_b32_e32 v7, v65
	v_mov_b32_e32 v6, v65
	v_mov_b32_e32 v5, v65
	v_mov_b32_e32 v4, v65
	v_mov_b32_e32 v3, v65
	v_mov_b32_e32 v2, v65
	s_cbranch_scc1 .LBB5_5
	s_mov_b32 s49, 0
	s_load_dword s36, s[0:1], 0x10
	s_load_dwordx4 s[28:31], s[0:1], 0x0
	s_load_dwordx4 s[32:35], s[0:1], 0x30
	s_load_dwordx2 s[46:47], s[0:1], 0x40
	s_mov_b32 s37, s18
	s_lshr_b32 s45, s18, 6
	s_mul_i32 s48, s49, s45
	s_lshl_b32 s48, s48, 7
	v_lshrrev_b32_e32 v98, 6, v0
	v_lshlrev_b32_e32 v98, 10, v98
	v_lshrrev_b32_e32 v222, 3, v0
	v_readfirstlane_b32 s44, v98
	v_and_b32_e32 v223, 7, v0
	v_and_b32_e32 v98, 7, v222
	v_xor_b32_e32 v223, v223, v98
	v_lshlrev_b32_e32 v223, 4, v223
	s_waitcnt lgkmcnt(0)
	s_lshl_b32 s38, s36, 6
	s_lshl_b32 s39, s36, 7
	s_add_u32 s40, s38, s39
	s_lshl_b32 s41, s37, 6
	s_lshl_b32 s42, s37, 7
	s_add_u32 s43, s41, s42
	s_mul_i32 s54, s3, s36
	s_lshl_b32 s54, s54, 1
	s_add_u32 s54, s54, s48
	s_add_u32 s28, s28, s54
	s_addc_u32 s29, s29, 0
	s_add_u32 s30, s30, s54
	s_addc_u32 s31, s31, 0
	s_mul_i32 s54, s49, s46
	s_mul_i32 s55, s16, s37
	s_add_u32 s54, s54, s55
	s_lshl_b32 s54, s54, 1
	s_add_u32 s54, s54, s48
	s_add_u32 s32, s32, s54
	s_addc_u32 s33, s33, 0
	s_add_u32 s34, s34, s54
	s_addc_u32 s35, s35, 0
	s_lshl_b32 s54, s36, 1
	s_lshl_b32 s55, s37, 1
	v_mul_lo_u32 v98, v222, s54
	v_mul_lo_u32 v222, v222, s55
	v_add_u32_e32 v223, v223, v222
	v_sub_u32_e32 v222, v223, v222
	v_add_u32_e32 v222, v222, v98
	v_and_b32_e32 v98, 15, v0
	v_lshrrev_b32_e32 v94, 1, v0
	v_and_b32_e32 v94, 64, v94
	v_or_b32_e32 v94, v94, v98
	v_lshlrev_b32_e32 v94, 7, v94
	v_lshlrev_b32_e32 v95, 7, v0
	v_and_b32_e32 v95, 0x2780, v95
	v_bfe_u32 v96, v0, 4, 2
	v_and_b32_e32 v97, 7, v0
	v_xor_b32_e32 v96, v96, v97
	v_lshlrev_b32_e32 v96, 4, v96
	v_xor_b32_e32 v97, 64, v96
	v_add_u32_e32 v98, v94, v97
	v_add_u32_e32 v97, v95, v97
	v_add_u32_e32 v94, v94, v96
	v_add_u32_e32 v95, v95, v96
	v_mov_b32_e32 v96, v98
	s_mov_b64 s[50:51], s[28:29]
	s_mov_b32 m0, s44
	s_nop 0
	global_load_lds_dwordx4 v222, s[50:51]
	s_mov_b64 s[52:53], s[32:33]
	s_add_u32 m0, s44, 0x4000
	s_nop 0
	global_load_lds_dwordx4 v223, s[52:53]
	s_mov_b64 s[50:51], s[30:31]
	s_add_u32 m0, s44, 0x8000
	s_nop 0
	global_load_lds_dwordx4 v222, s[50:51]
	s_mov_b64 s[52:53], s[34:35]
	s_add_u32 m0, s44, 0xc000
	s_nop 0
	global_load_lds_dwordx4 v223, s[52:53]
	s_add_u32 s50, s28, s38
	s_addc_u32 s51, s29, 0
	s_add_u32 m0, s44, 0x1000
	s_nop 0
	global_load_lds_dwordx4 v222, s[50:51]
	s_add_u32 s52, s32, s41
	s_addc_u32 s53, s33, 0
	s_add_u32 m0, s44, 0x5000
	s_nop 0
	global_load_lds_dwordx4 v223, s[52:53]
	s_add_u32 s50, s30, s38
	s_addc_u32 s51, s31, 0
	s_add_u32 m0, s44, 0x9000
	s_nop 0
	global_load_lds_dwordx4 v222, s[50:51]
	s_add_u32 s52, s34, s41
	s_addc_u32 s53, s35, 0
	s_add_u32 m0, s44, 0xd000
	s_nop 0
	global_load_lds_dwordx4 v223, s[52:53]
	s_add_u32 s50, s28, s39
	s_addc_u32 s51, s29, 0
	s_add_u32 m0, s44, 0x2000
	s_nop 0
	global_load_lds_dwordx4 v222, s[50:51]
	s_add_u32 s52, s32, s42
	s_addc_u32 s53, s33, 0
	s_add_u32 m0, s44, 0x6000
	s_nop 0
	global_load_lds_dwordx4 v223, s[52:53]
	s_add_u32 s50, s30, s39
	s_addc_u32 s51, s31, 0
	s_add_u32 m0, s44, 0xa000
	s_nop 0
	global_load_lds_dwordx4 v222, s[50:51]
	s_add_u32 s52, s34, s42
	s_addc_u32 s53, s35, 0
	s_add_u32 m0, s44, 0xe000
	s_nop 0
	global_load_lds_dwordx4 v223, s[52:53]
	s_add_u32 s50, s28, s40
	s_addc_u32 s51, s29, 0
	s_add_u32 m0, s44, 0x3000
	s_nop 0
	global_load_lds_dwordx4 v222, s[50:51]
	s_add_u32 s52, s32, s43
	s_addc_u32 s53, s33, 0
	s_add_u32 m0, s44, 0x7000
	s_nop 0
	global_load_lds_dwordx4 v223, s[52:53]
	s_add_u32 s50, s30, s40
	s_addc_u32 s51, s31, 0
	s_add_u32 m0, s44, 0xb000
	s_nop 0
	global_load_lds_dwordx4 v222, s[50:51]
	s_add_u32 s52, s34, s43
	s_addc_u32 s53, s35, 0
	s_add_u32 m0, s44, 0xf000
	s_nop 0
	global_load_lds_dwordx4 v223, s[52:53]

.Llast_k5:
	v_mfma_f32_16x16x32_f16 v[14:17], v[122:125], v[130:133], v[14:17]
	v_mfma_f32_16x16x32_f16 v[14:17], v[122:125], v[134:137], v[14:17]
	v_mfma_f32_16x16x32_f16 v[14:17], v[126:129], v[130:133], v[14:17]
	v_mfma_f32_16x16x32_f16 v[10:13], v[122:125], v[138:141], v[10:13]
	v_mfma_f32_16x16x32_f16 v[10:13], v[122:125], v[142:145], v[10:13]
	v_mfma_f32_16x16x32_f16 v[10:13], v[126:129], v[138:141], v[10:13]
	v_mfma_f32_16x16x32_f16 v[6:9], v[122:125], v[146:149], v[6:9]
	v_mfma_f32_16x16x32_f16 v[6:9], v[122:125], v[150:153], v[6:9]
	v_mfma_f32_16x16x32_f16 v[6:9], v[126:129], v[146:149], v[6:9]
	v_mfma_f32_16x16x32_f16 v[2:5], v[122:125], v[154:157], v[2:5]
	v_mfma_f32_16x16x32_f16 v[2:5], v[122:125], v[158:161], v[2:5]
	v_mfma_f32_16x16x32_f16 v[2:5], v[126:129], v[154:157], v[2:5]
	s_waitcnt lgkmcnt(7)
	v_mfma_f32_16x16x32_f16 v[62:65], v[162:165], v[194:197], v[62:65]
	s_waitcnt lgkmcnt(6)
	v_mfma_f32_16x16x32_f16 v[62:65], v[162:165], v[198:201], v[62:65]
	v_mfma_f32_16x16x32_f16 v[62:65], v[166:169], v[194:197], v[62:65]
	s_waitcnt lgkmcnt(5)
	v_mfma_f32_16x16x32_f16 v[58:61], v[162:165], v[202:205], v[58:61]
	s_waitcnt lgkmcnt(4)
	v_mfma_f32_16x16x32_f16 v[58:61], v[162:165], v[206:209], v[58:61]
	v_mfma_f32_16x16x32_f16 v[58:61], v[166:169], v[202:205], v[58:61]
	s_waitcnt lgkmcnt(3)
	v_mfma_f32_16x16x32_f16 v[54:57], v[162:165], v[210:213], v[54:57]
	s_waitcnt lgkmcnt(2)
	v_mfma_f32_16x16x32_f16 v[54:57], v[162:165], v[214:217], v[54:57]
	v_mfma_f32_16x16x32_f16 v[54:57], v[166:169], v[210:213], v[54:57]
	s_waitcnt lgkmcnt(1)
	v_mfma_f32_16x16x32_f16 v[50:53], v[162:165], v[98:101], v[50:53]
	s_waitcnt lgkmcnt(0)
	v_mfma_f32_16x16x32_f16 v[50:53], v[162:165], v[218:221], v[50:53]
	v_mfma_f32_16x16x32_f16 v[50:53], v[166:169], v[98:101], v[50:53]
	v_mfma_f32_16x16x32_f16 v[46:49], v[170:173], v[194:197], v[46:49]
	v_mfma_f32_16x16x32_f16 v[46:49], v[170:173], v[198:201], v[46:49]
	v_mfma_f32_16x16x32_f16 v[46:49], v[174:177], v[194:197], v[46:49]
	v_mfma_f32_16x16x32_f16 v[42:45], v[170:173], v[202:205], v[42:45]
	v_mfma_f32_16x16x32_f16 v[42:45], v[170:173], v[206:209], v[42:45]
	v_mfma_f32_16x16x32_f16 v[42:45], v[174:177], v[202:205], v[42:45]
	v_mfma_f32_16x16x32_f16 v[38:41], v[170:173], v[210:213], v[38:41]
	v_mfma_f32_16x16x32_f16 v[38:41], v[170:173], v[214:217], v[38:41]
	v_mfma_f32_16x16x32_f16 v[38:41], v[174:177], v[210:213], v[38:41]
	v_mfma_f32_16x16x32_f16 v[34:37], v[170:173], v[98:101], v[34:37]
	v_mfma_f32_16x16x32_f16 v[34:37], v[170:173], v[218:221], v[34:37]
	v_mfma_f32_16x16x32_f16 v[34:37], v[174:177], v[98:101], v[34:37]
	v_mfma_f32_16x16x32_f16 v[30:33], v[178:181], v[194:197], v[30:33]
	v_mfma_f32_16x16x32_f16 v[30:33], v[178:181], v[198:201], v[30:33]
	v_mfma_f32_16x16x32_f16 v[30:33], v[182:185], v[194:197], v[30:33]
	v_mfma_f32_16x16x32_f16 v[26:29], v[178:181], v[202:205], v[26:29]
	v_mfma_f32_16x16x32_f16 v[26:29], v[178:181], v[206:209], v[26:29]
	v_mfma_f32_16x16x32_f16 v[26:29], v[182:185], v[202:205], v[26:29]
	v_mfma_f32_16x16x32_f16 v[22:25], v[178:181], v[210:213], v[22:25]
	v_mfma_f32_16x16x32_f16 v[22:25], v[178:181], v[214:217], v[22:25]
	v_mfma_f32_16x16x32_f16 v[22:25], v[182:185], v[210:213], v[22:25]
	v_mfma_f32_16x16x32_f16 v[18:21], v[178:181], v[98:101], v[18:21]
	v_mfma_f32_16x16x32_f16 v[18:21], v[178:181], v[218:221], v[18:21]
	v_mfma_f32_16x16x32_f16 v[18:21], v[182:185], v[98:101], v[18:21]
	v_mfma_f32_16x16x32_f16 v[14:17], v[186:189], v[194:197], v[14:17]
	v_mfma_f32_16x16x32_f16 v[14:17], v[186:189], v[198:201], v[14:17]
	v_mfma_f32_16x16x32_f16 v[14:17], v[190:193], v[194:197], v[14:17]
	v_mfma_f32_16x16x32_f16 v[10:13], v[186:189], v[202:205], v[10:13]
	v_mfma_f32_16x16x32_f16 v[10:13], v[186:189], v[206:209], v[10:13]
	v_mfma_f32_16x16x32_f16 v[10:13], v[190:193], v[202:205], v[10:13]
	v_mfma_f32_16x16x32_f16 v[6:9], v[186:189], v[210:213], v[6:9]
	v_mfma_f32_16x16x32_f16 v[6:9], v[186:189], v[214:217], v[6:9]
	v_mfma_f32_16x16x32_f16 v[6:9], v[190:193], v[210:213], v[6:9]
	v_mfma_f32_16x16x32_f16 v[2:5], v[186:189], v[98:101], v[2:5]
	v_mfma_f32_16x16x32_f16 v[2:5], v[186:189], v[218:221], v[2:5]
	v_mfma_f32_16x16x32_f16 v[2:5], v[190:193], v[98:101], v[2:5]
.LBB5_5:
	v_lshlrev_b32_e32 v66, 7, v0
	s_and_b32 s0, s16, 0x180
	v_and_b32_e32 v74, 0x6000, v66
	v_and_or_b32 v66, v0, 64, s0
	v_add_u32_e32 v1, s3, v1
	v_lshrrev_b32_e32 v66, 6, v66
	v_ashrrev_i32_e32 v67, 7, v1
	v_and_b32_e32 v68, 63, v0
	v_and_or_b32 v66, v67, -8, v66
	v_bfe_u32 v73, v0, 4, 2
	v_and_b32_e32 v75, 0x3c0, v1
	s_mov_b64 s[0:1], -1
	s_cmp_gt_i32 s2, 7
	v_ashrrev_i32_e32 v67, 31, v66
	v_and_b32_e32 v76, 7, v0
	v_lshrrev_b32_e32 v72, 3, v68
	s_cbranch_scc1 .LBB5_8
	s_andn2_b64 vcc, exec, s[0:1]
	s_cbranch_vccz .LBB5_9

	.amdhsa_kernel _Z12gemm2_kernelILi3ELi0ELb0ELi4ELi4EEv2GP
		.amdhsa_group_segment_fixed_size 65536
		.amdhsa_private_segment_fixed_size 0
		.amdhsa_kernarg_size 440
		.amdhsa_user_sgpr_count 2
		.amdhsa_user_sgpr_dispatch_ptr 0
		.amdhsa_user_sgpr_queue_ptr 0
		.amdhsa_user_sgpr_kernarg_segment_ptr 1
		.amdhsa_user_sgpr_dispatch_id 0
		.amdhsa_user_sgpr_kernarg_preload_length 0
		.amdhsa_user_sgpr_kernarg_preload_offset 0
		.amdhsa_user_sgpr_private_segment_size 0
		.amdhsa_uses_dynamic_stack 0
		.amdhsa_enable_private_segment 0
		.amdhsa_system_sgpr_workgroup_id_x 1
		.amdhsa_system_sgpr_workgroup_id_y 1
		.amdhsa_system_sgpr_workgroup_id_z 0
		.amdhsa_system_sgpr_workgroup_info 0
		.amdhsa_system_vgpr_workitem_id 0
		.amdhsa_next_free_vgpr 224
		.amdhsa_next_free_sgpr 96
		.amdhsa_accum_offset 224
		.amdhsa_reserve_vcc 1
		.amdhsa_float_round_mode_32 0
		.amdhsa_float_round_mode_16_64 0
		.amdhsa_float_denorm_mode_32 3
		.amdhsa_float_denorm_mode_16_64 3
		.amdhsa_dx10_clamp 1
		.amdhsa_ieee_mode 1
		.amdhsa_fp16_overflow 0
		.amdhsa_tg_split 0
		.amdhsa_exception_fp_ieee_invalid_op 0
		.amdhsa_exception_fp_denorm_src 0
		.amdhsa_exception_fp_ieee_div_zero 0
		.amdhsa_exception_fp_ieee_overflow 0
		.amdhsa_exception_fp_ieee_underflow 0
		.amdhsa_exception_fp_ieee_inexact 0
		.amdhsa_exception_int_div_zero 0
	.end_amdhsa_kernel

.Lloop_k6:
	s_waitcnt vmcnt(0)
	s_barrier
	s_add_i32 s45, s45, -1
	s_cmp_eq_u32 s45, 0
	s_cbranch_scc1 .Llast0_k6
	s_add_u32 s28, s28, 0x80
	s_addc_u32 s29, s29, 0
	s_add_u32 s30, s30, 0x80
	s_addc_u32 s31, s31, 0
	s_add_u32 s32, s32, 0x80
	s_addc_u32 s33, s33, 0
	s_add_u32 s34, s34, 0x80
	s_addc_u32 s35, s35, 0
	s_mov_b64 s[50:51], s[28:29]
	s_add_u32 m0, s44, 0x10000
	ds_read_b128 v[98:101], v94
	ds_read_b128 v[102:105], v94 offset:32768
	ds_read_b128 v[106:109], v94 offset:2048
	ds_read_b128 v[110:113], v94 offset:34816
	ds_read_b128 v[114:117], v94 offset:4096
	ds_read_b128 v[118:121], v94 offset:36864
	ds_read_b128 v[122:125], v94 offset:6144
	ds_read_b128 v[126:129], v94 offset:38912
	ds_read_b128 v[130:133], v95 offset:16384
	ds_read_b128 v[134:137], v95 offset:49152
	s_waitcnt lgkmcnt(1)
	v_mfma_f32_16x16x32_f16 v[62:65], v[98:101], v[130:133], v[62:65]
	global_load_lds_dwordx4 v222, s[50:51]
	ds_read_b128 v[138:141], v95 offset:18432
	ds_read_b128 v[142:145], v95 offset:51200
	s_waitcnt lgkmcnt(2)
	v_mfma_f32_16x16x32_f16 v[62:65], v[98:101], v[134:137], v[62:65]
	ds_read_b128 v[146:149], v95 offset:20480
	ds_read_b128 v[150:153], v95 offset:53248
	v_mfma_f32_16x16x32_f16 v[62:65], v[102:105], v[130:133], v[62:65]
	s_mov_b64 s[52:53], s[32:33]
	s_add_u32 m0, s44, 0x14000
	ds_read_b128 v[154:157], v95 offset:22528
	ds_read_b128 v[158:161], v95 offset:55296
	s_waitcnt lgkmcnt(5)
	v_mfma_f32_16x16x32_f16 v[58:61], v[98:101], v[138:141], v[58:61]
	global_load_lds_dwordx4 v223, s[52:53]
	ds_read_b128 v[162:165], v96
	ds_read_b128 v[166:169], v96 offset:32768
	s_waitcnt lgkmcnt(6)
	v_mfma_f32_16x16x32_f16 v[58:61], v[98:101], v[142:145], v[58:61]
	ds_read_b128 v[170:173], v96 offset:2048
	ds_read_b128 v[174:177], v96 offset:34816
	v_mfma_f32_16x16x32_f16 v[58:61], v[102:105], v[138:141], v[58:61]
	s_mov_b64 s[50:51], s[30:31]
	s_add_u32 m0, s44, 0x18000
	ds_read_b128 v[178:181], v96 offset:4096
	ds_read_b128 v[182:185], v96 offset:36864
	s_waitcnt lgkmcnt(9)
	v_mfma_f32_16x16x32_f16 v[54:57], v[98:101], v[146:149], v[54:57]
	global_load_lds_dwordx4 v222, s[50:51]
	ds_read_b128 v[186:189], v96 offset:6144
	ds_read_b128 v[190:193], v96 offset:38912
	s_waitcnt lgkmcnt(10)
	v_mfma_f32_16x16x32_f16 v[54:57], v[98:101], v[150:153], v[54:57]
	ds_read_b128 v[194:197], v97 offset:16384
	ds_read_b128 v[198:201], v97 offset:49152
	v_mfma_f32_16x16x32_f16 v[54:57], v[102:105], v[146:149], v[54:57]
	s_mov_b64 s[52:53], s[34:35]
	s_add_u32 m0, s44, 0x1c000
	ds_read_b128 v[202:205], v97 offset:18432
	ds_read_b128 v[206:209], v97 offset:51200
	s_waitcnt lgkmcnt(13)
	v_mfma_f32_16x16x32_f16 v[50:53], v[98:101], v[154:157], v[50:53]
	global_load_lds_dwordx4 v223, s[52:53]
	ds_read_b128 v[210:213], v97 offset:20480
	ds_read_b128 v[214:217], v97 offset:53248
	s_waitcnt lgkmcnt(14)
	v_mfma_f32_16x16x32_f16 v[50:53], v[98:101], v[158:161], v[50:53]
	ds_read_b128 v[98:101], v97 offset:22528
	ds_read_b128 v[218:221], v97 offset:55296
	v_mfma_f32_16x16x32_f16 v[50:53], v[102:105], v[154:157], v[50:53]
	s_add_u32 s50, s28, s38
	s_addc_u32 s51, s29, 0
	s_add_u32 m0, s44, 0x11000
	v_mfma_f32_16x16x32_f16 v[46:49], v[106:109], v[130:133], v[46:49]
	global_load_lds_dwordx4 v222, s[50:51]
	v_mfma_f32_16x16x32_f16 v[46:49], v[106:109], v[134:137], v[46:49]
	v_mfma_f32_16x16x32_f16 v[46:49], v[110:113], v[130:133], v[46:49]
	s_add_u32 s52, s32, s41
	s_addc_u32 s53, s33, 0
	s_add_u32 m0, s44, 0x15000
	v_mfma_f32_16x16x32_f16 v[42:45], v[106:109], v[138:141], v[42:45]
	global_load_lds_dwordx4 v223, s[52:53]
	v_mfma_f32_16x16x32_f16 v[42:45], v[106:109], v[142:145], v[42:45]
	v_mfma_f32_16x16x32_f16 v[42:45], v[110:113], v[138:141], v[42:45]
	s_add_u32 s50, s30, s38
	s_addc_u32 s51, s31, 0
	s_add_u32 m0, s44, 0x19000
	v_mfma_f32_16x16x32_f16 v[38:41], v[106:109], v[146:149], v[38:41]
	global_load_lds_dwordx4 v222, s[50:51]
	v_mfma_f32_16x16x32_f16 v[38:41], v[106:109], v[150:153], v[38:41]
	v_mfma_f32_16x16x32_f16 v[38:41], v[110:113], v[146:149], v[38:41]
	s_add_u32 s52, s34, s41
	s_addc_u32 s53, s35, 0
	s_add_u32 m0, s44, 0x1d000
	v_mfma_f32_16x16x32_f16 v[34:37], v[106:109], v[154:157], v[34:37]
	global_load_lds_dwordx4 v223, s[52:53]
	v_mfma_f32_16x16x32_f16 v[34:37], v[106:109], v[158:161], v[34:37]
	v_mfma_f32_16x16x32_f16 v[34:37], v[110:113], v[154:157], v[34:37]
	s_add_u32 s50, s28, s39
	s_addc_u32 s51, s29, 0
	s_add_u32 m0, s44, 0x12000
	v_mfma_f32_16x16x32_f16 v[30:33], v[114:117], v[130:133], v[30:33]
	global_load_lds_dwordx4 v222, s[50:51]
	v_mfma_f32_16x16x32_f16 v[30:33], v[114:117], v[134:137], v[30:33]
	v_mfma_f32_16x16x32_f16 v[30:33], v[118:121], v[130:133], v[30:33]
	s_add_u32 s52, s32, s42
	s_addc_u32 s53, s33, 0
	s_add_u32 m0, s44, 0x16000
	v_mfma_f32_16x16x32_f16 v[26:29], v[114:117], v[138:141], v[26:29]
	global_load_lds_dwordx4 v223, s[52:53]
	v_mfma_f32_16x16x32_f16 v[26:29], v[114:117], v[142:145], v[26:29]
	v_mfma_f32_16x16x32_f16 v[26:29], v[118:121], v[138:141], v[26:29]
	s_add_u32 s50, s30, s39
	s_addc_u32 s51, s31, 0
	s_add_u32 m0, s44, 0x1a000
	v_mfma_f32_16x16x32_f16 v[22:25], v[114:117], v[146:149], v[22:25]
	global_load_lds_dwordx4 v222, s[50:51]
	v_mfma_f32_16x16x32_f16 v[22:25], v[114:117], v[150:153], v[22:25]
	v_mfma_f32_16x16x32_f16 v[22:25], v[118:121], v[146:149], v[22:25]
	s_add_u32 s52, s34, s42
	s_addc_u32 s53, s35, 0
	s_add_u32 m0, s44, 0x1e000
	v_mfma_f32_16x16x32_f16 v[18:21], v[114:117], v[154:157], v[18:21]
	global_load_lds_dwordx4 v223, s[52:53]
	v_mfma_f32_16x16x32_f16 v[18:21], v[114:117], v[158:161], v[18:21]
	v_mfma_f32_16x16x32_f16 v[18:21], v[118:121], v[154:157], v[18:21]
	s_add_u32 s50, s28, s40
	s_addc_u32 s51, s29, 0
	s_add_u32 m0, s44, 0x13000
	v_mfma_f32_16x16x32_f16 v[14:17], v[122:125], v[130:133], v[14:17]
	global_load_lds_dwordx4 v222, s[50:51]
	v_mfma_f32_16x16x32_f16 v[14:17], v[122:125], v[134:137], v[14:17]
	v_mfma_f32_16x16x32_f16 v[14:17], v[126:129], v[130:133], v[14:17]
	s_add_u32 s52, s32, s43
	s_addc_u32 s53, s33, 0
	s_add_u32 m0, s44, 0x17000
	v_mfma_f32_16x16x32_f16 v[10:13], v[122:125], v[138:141], v[10:13]
	global_load_lds_dwordx4 v223, s[52:53]
	v_mfma_f32_16x16x32_f16 v[10:13], v[122:125], v[142:145], v[10:13]
	v_mfma_f32_16x16x32_f16 v[10:13], v[126:129], v[138:141], v[10:13]
	s_add_u32 s50, s30, s40
	s_addc_u32 s51, s31, 0
	s_add_u32 m0, s44, 0x1b000
	v_mfma_f32_16x16x32_f16 v[6:9], v[122:125], v[146:149], v[6:9]
	global_load_lds_dwordx4 v222, s[50:51]
	v_mfma_f32_16x16x32_f16 v[6:9], v[122:125], v[150:153], v[6:9]
	v_mfma_f32_16x16x32_f16 v[6:9], v[126:129], v[146:149], v[6:9]
	s_add_u32 s52, s34, s43
	s_addc_u32 s53, s35, 0
	s_add_u32 m0, s44, 0x1f000
	v_mfma_f32_16x16x32_f16 v[2:5], v[122:125], v[154:157], v[2:5]
	global_load_lds_dwordx4 v223, s[52:53]
	v_mfma_f32_16x16x32_f16 v[2:5], v[122:125], v[158:161], v[2:5]
	v_mfma_f32_16x16x32_f16 v[2:5], v[126:129], v[154:157], v[2:5]
	s_waitcnt lgkmcnt(7)
	v_mfma_f32_16x16x32_f16 v[62:65], v[162:165], v[194:197], v[62:65]
	s_waitcnt lgkmcnt(6)
	v_mfma_f32_16x16x32_f16 v[62:65], v[162:165], v[198:201], v[62:65]
	v_mfma_f32_16x16x32_f16 v[62:65], v[166:169], v[194:197], v[62:65]
	s_waitcnt lgkmcnt(5)
	v_mfma_f32_16x16x32_f16 v[58:61], v[162:165], v[202:205], v[58:61]
	s_waitcnt lgkmcnt(4)
	v_mfma_f32_16x16x32_f16 v[58:61], v[162:165], v[206:209], v[58:61]
	v_mfma_f32_16x16x32_f16 v[58:61], v[166:169], v[202:205], v[58:61]
	s_waitcnt lgkmcnt(3)
	v_mfma_f32_16x16x32_f16 v[54:57], v[162:165], v[210:213], v[54:57]
	s_waitcnt lgkmcnt(2)
	v_mfma_f32_16x16x32_f16 v[54:57], v[162:165], v[214:217], v[54:57]
	v_mfma_f32_16x16x32_f16 v[54:57], v[166:169], v[210:213], v[54:57]
	s_waitcnt lgkmcnt(1)
	v_mfma_f32_16x16x32_f16 v[50:53], v[162:165], v[98:101], v[50:53]
	s_waitcnt lgkmcnt(0)
	v_mfma_f32_16x16x32_f16 v[50:53], v[162:165], v[218:221], v[50:53]
	v_mfma_f32_16x16x32_f16 v[50:53], v[166:169], v[98:101], v[50:53]
	v_mfma_f32_16x16x32_f16 v[46:49], v[170:173], v[194:197], v[46:49]
	v_mfma_f32_16x16x32_f16 v[46:49], v[170:173], v[198:201], v[46:49]
	v_mfma_f32_16x16x32_f16 v[46:49], v[174:177], v[194:197], v[46:49]
	v_mfma_f32_16x16x32_f16 v[42:45], v[170:173], v[202:205], v[42:45]
	v_mfma_f32_16x16x32_f16 v[42:45], v[170:173], v[206:209], v[42:45]
	v_mfma_f32_16x16x32_f16 v[42:45], v[174:177], v[202:205], v[42:45]
	v_mfma_f32_16x16x32_f16 v[38:41], v[170:173], v[210:213], v[38:41]
	v_mfma_f32_16x16x32_f16 v[38:41], v[170:173], v[214:217], v[38:41]
	v_mfma_f32_16x16x32_f16 v[38:41], v[174:177], v[210:213], v[38:41]
	v_mfma_f32_16x16x32_f16 v[34:37], v[170:173], v[98:101], v[34:37]
	v_mfma_f32_16x16x32_f16 v[34:37], v[170:173], v[218:221], v[34:37]
	v_mfma_f32_16x16x32_f16 v[34:37], v[174:177], v[98:101], v[34:37]
	v_mfma_f32_16x16x32_f16 v[30:33], v[178:181], v[194:197], v[30:33]
	v_mfma_f32_16x16x32_f16 v[30:33], v[178:181], v[198:201], v[30:33]
	v_mfma_f32_16x16x32_f16 v[30:33], v[182:185], v[194:197], v[30:33]
	v_mfma_f32_16x16x32_f16 v[26:29], v[178:181], v[202:205], v[26:29]
	v_mfma_f32_16x16x32_f16 v[26:29], v[178:181], v[206:209], v[26:29]
	v_mfma_f32_16x16x32_f16 v[26:29], v[182:185], v[202:205], v[26:29]
	v_mfma_f32_16x16x32_f16 v[22:25], v[178:181], v[210:213], v[22:25]
	v_mfma_f32_16x16x32_f16 v[22:25], v[178:181], v[214:217], v[22:25]
	v_mfma_f32_16x16x32_f16 v[22:25], v[182:185], v[210:213], v[22:25]
	v_mfma_f32_16x16x32_f16 v[18:21], v[178:181], v[98:101], v[18:21]
	v_mfma_f32_16x16x32_f16 v[18:21], v[178:181], v[218:221], v[18:21]
	v_mfma_f32_16x16x32_f16 v[18:21], v[182:185], v[98:101], v[18:21]
	v_mfma_f32_16x16x32_f16 v[14:17], v[186:189], v[194:197], v[14:17]
	v_mfma_f32_16x16x32_f16 v[14:17], v[186:189], v[198:201], v[14:17]
	v_mfma_f32_16x16x32_f16 v[14:17], v[190:193], v[194:197], v[14:17]
	v_mfma_f32_16x16x32_f16 v[10:13], v[186:189], v[202:205], v[10:13]
	v_mfma_f32_16x16x32_f16 v[10:13], v[186:189], v[206:209], v[10:13]
	v_mfma_f32_16x16x32_f16 v[10:13], v[190:193], v[202:205], v[10:13]
	v_mfma_f32_16x16x32_f16 v[6:9], v[186:189], v[210:213], v[6:9]
	v_mfma_f32_16x16x32_f16 v[6:9], v[186:189], v[214:217], v[6:9]
	v_mfma_f32_16x16x32_f16 v[6:9], v[190:193], v[210:213], v[6:9]
	v_mfma_f32_16x16x32_f16 v[2:5], v[186:189], v[98:101], v[2:5]
	v_mfma_f32_16x16x32_f16 v[2:5], v[186:189], v[218:221], v[2:5]
	v_mfma_f32_16x16x32_f16 v[2:5], v[190:193], v[98:101], v[2:5]
	s_waitcnt vmcnt(0)
	s_barrier
	s_add_i32 s45, s45, -1
	s_cmp_eq_u32 s45, 0
	s_cbranch_scc1 .Llast1_k6
	s_add_u32 s28, s28, 0x80
	s_addc_u32 s29, s29, 0
	s_add_u32 s30, s30, 0x80
	s_addc_u32 s31, s31, 0
	s_add_u32 s32, s32, 0x80
	s_addc_u32 s33, s33, 0
	s_add_u32 s34, s34, 0x80
	s_addc_u32 s35, s35, 0
	s_mov_b64 s[50:51], s[28:29]
	s_mov_b32 m0, s44
	ds_read_b128 v[98:101], v224
	ds_read_b128 v[102:105], v224 offset:32768
	ds_read_b128 v[106:109], v224 offset:2048
	ds_read_b128 v[110:113], v224 offset:34816
	ds_read_b128 v[114:117], v224 offset:4096
	ds_read_b128 v[118:121], v224 offset:36864
	ds_read_b128 v[122:125], v224 offset:6144
	ds_read_b128 v[126:129], v224 offset:38912
	ds_read_b128 v[130:133], v225 offset:16384
	ds_read_b128 v[134:137], v225 offset:49152
	s_waitcnt lgkmcnt(1)
	v_mfma_f32_16x16x32_f16 v[62:65], v[98:101], v[130:133], v[62:65]
	global_load_lds_dwordx4 v222, s[50:51]
	ds_read_b128 v[138:141], v225 offset:18432
	ds_read_b128 v[142:145], v225 offset:51200
	s_waitcnt lgkmcnt(2)
	v_mfma_f32_16x16x32_f16 v[62:65], v[98:101], v[134:137], v[62:65]
	ds_read_b128 v[146:149], v225 offset:20480
	ds_read_b128 v[150:153], v225 offset:53248
	v_mfma_f32_16x16x32_f16 v[62:65], v[102:105], v[130:133], v[62:65]
	s_mov_b64 s[52:53], s[32:33]
	s_add_u32 m0, s44, 0x4000
	ds_read_b128 v[154:157], v225 offset:22528
	ds_read_b128 v[158:161], v225 offset:55296
	s_waitcnt lgkmcnt(5)
	v_mfma_f32_16x16x32_f16 v[58:61], v[98:101], v[138:141], v[58:61]
	global_load_lds_dwordx4 v223, s[52:53]
	ds_read_b128 v[162:165], v226
	ds_read_b128 v[166:169], v226 offset:32768
	s_waitcnt lgkmcnt(6)
	v_mfma_f32_16x16x32_f16 v[58:61], v[98:101], v[142:145], v[58:61]
	ds_read_b128 v[170:173], v226 offset:2048
	ds_read_b128 v[174:177], v226 offset:34816
	v_mfma_f32_16x16x32_f16 v[58:61], v[102:105], v[138:141], v[58:61]
	s_mov_b64 s[50:51], s[30:31]
	s_add_u32 m0, s44, 0x8000
	ds_read_b128 v[178:181], v226 offset:4096
	ds_read_b128 v[182:185], v226 offset:36864
	s_waitcnt lgkmcnt(9)
	v_mfma_f32_16x16x32_f16 v[54:57], v[98:101], v[146:149], v[54:57]
	global_load_lds_dwordx4 v222, s[50:51]
	ds_read_b128 v[186:189], v226 offset:6144
	ds_read_b128 v[190:193], v226 offset:38912
	s_waitcnt lgkmcnt(10)
	v_mfma_f32_16x16x32_f16 v[54:57], v[98:101], v[150:153], v[54:57]
	ds_read_b128 v[194:197], v227 offset:16384
	ds_read_b128 v[198:201], v227 offset:49152
	v_mfma_f32_16x16x32_f16 v[54:57], v[102:105], v[146:149], v[54:57]
	s_mov_b64 s[52:53], s[34:35]
	s_add_u32 m0, s44, 0xc000
	ds_read_b128 v[202:205], v227 offset:18432
	ds_read_b128 v[206:209], v227 offset:51200
	s_waitcnt lgkmcnt(13)
	v_mfma_f32_16x16x32_f16 v[50:53], v[98:101], v[154:157], v[50:53]
	global_load_lds_dwordx4 v223, s[52:53]
	ds_read_b128 v[210:213], v227 offset:20480
	ds_read_b128 v[214:217], v227 offset:53248
	s_waitcnt lgkmcnt(14)
	v_mfma_f32_16x16x32_f16 v[50:53], v[98:101], v[158:161], v[50:53]
	ds_read_b128 v[98:101], v227 offset:22528
	ds_read_b128 v[218:221], v227 offset:55296
	v_mfma_f32_16x16x32_f16 v[50:53], v[102:105], v[154:157], v[50:53]
	s_add_u32 s50, s28, s38
	s_addc_u32 s51, s29, 0
	s_add_u32 m0, s44, 0x1000
	v_mfma_f32_16x16x32_f16 v[46:49], v[106:109], v[130:133], v[46:49]
	global_load_lds_dwordx4 v222, s[50:51]
	v_mfma_f32_16x16x32_f16 v[46:49], v[106:109], v[134:137], v[46:49]
	v_mfma_f32_16x16x32_f16 v[46:49], v[110:113], v[130:133], v[46:49]
	s_add_u32 s52, s32, s41
	s_addc_u32 s53, s33, 0
	s_add_u32 m0, s44, 0x5000
	v_mfma_f32_16x16x32_f16 v[42:45], v[106:109], v[138:141], v[42:45]
	global_load_lds_dwordx4 v223, s[52:53]
	v_mfma_f32_16x16x32_f16 v[42:45], v[106:109], v[142:145], v[42:45]
	v_mfma_f32_16x16x32_f16 v[42:45], v[110:113], v[138:141], v[42:45]
	s_add_u32 s50, s30, s38
	s_addc_u32 s51, s31, 0
	s_add_u32 m0, s44, 0x9000
	v_mfma_f32_16x16x32_f16 v[38:41], v[106:109], v[146:149], v[38:41]
	global_load_lds_dwordx4 v222, s[50:51]
	v_mfma_f32_16x16x32_f16 v[38:41], v[106:109], v[150:153], v[38:41]
	v_mfma_f32_16x16x32_f16 v[38:41], v[110:113], v[146:149], v[38:41]
	s_add_u32 s52, s34, s41
	s_addc_u32 s53, s35, 0
	s_add_u32 m0, s44, 0xd000
	v_mfma_f32_16x16x32_f16 v[34:37], v[106:109], v[154:157], v[34:37]
	global_load_lds_dwordx4 v223, s[52:53]
	v_mfma_f32_16x16x32_f16 v[34:37], v[106:109], v[158:161], v[34:37]
	v_mfma_f32_16x16x32_f16 v[34:37], v[110:113], v[154:157], v[34:37]
	s_add_u32 s50, s28, s39
	s_addc_u32 s51, s29, 0
	s_add_u32 m0, s44, 0x2000
	v_mfma_f32_16x16x32_f16 v[30:33], v[114:117], v[130:133], v[30:33]
	global_load_lds_dwordx4 v222, s[50:51]
	v_mfma_f32_16x16x32_f16 v[30:33], v[114:117], v[134:137], v[30:33]
	v_mfma_f32_16x16x32_f16 v[30:33], v[118:121], v[130:133], v[30:33]
	s_add_u32 s52, s32, s42
	s_addc_u32 s53, s33, 0
	s_add_u32 m0, s44, 0x6000
	v_mfma_f32_16x16x32_f16 v[26:29], v[114:117], v[138:141], v[26:29]
	global_load_lds_dwordx4 v223, s[52:53]
	v_mfma_f32_16x16x32_f16 v[26:29], v[114:117], v[142:145], v[26:29]
	v_mfma_f32_16x16x32_f16 v[26:29], v[118:121], v[138:141], v[26:29]
	s_add_u32 s50, s30, s39
	s_addc_u32 s51, s31, 0
	s_add_u32 m0, s44, 0xa000
	v_mfma_f32_16x16x32_f16 v[22:25], v[114:117], v[146:149], v[22:25]
	global_load_lds_dwordx4 v222, s[50:51]
	v_mfma_f32_16x16x32_f16 v[22:25], v[114:117], v[150:153], v[22:25]
	v_mfma_f32_16x16x32_f16 v[22:25], v[118:121], v[146:149], v[22:25]
	s_add_u32 s52, s34, s42
	s_addc_u32 s53, s35, 0
	s_add_u32 m0, s44, 0xe000
	v_mfma_f32_16x16x32_f16 v[18:21], v[114:117], v[154:157], v[18:21]
	global_load_lds_dwordx4 v223, s[52:53]
	v_mfma_f32_16x16x32_f16 v[18:21], v[114:117], v[158:161], v[18:21]
	v_mfma_f32_16x16x32_f16 v[18:21], v[118:121], v[154:157], v[18:21]
	s_add_u32 s50, s28, s40
	s_addc_u32 s51, s29, 0
	s_add_u32 m0, s44, 0x3000
	v_mfma_f32_16x16x32_f16 v[14:17], v[122:125], v[130:133], v[14:17]
	global_load_lds_dwordx4 v222, s[50:51]
	v_mfma_f32_16x16x32_f16 v[14:17], v[122:125], v[134:137], v[14:17]
	v_mfma_f32_16x16x32_f16 v[14:17], v[126:129], v[130:133], v[14:17]
	s_add_u32 s52, s32, s43
	s_addc_u32 s53, s33, 0
	s_add_u32 m0, s44, 0x7000
	v_mfma_f32_16x16x32_f16 v[10:13], v[122:125], v[138:141], v[10:13]
	global_load_lds_dwordx4 v223, s[52:53]
	v_mfma_f32_16x16x32_f16 v[10:13], v[122:125], v[142:145], v[10:13]
	v_mfma_f32_16x16x32_f16 v[10:13], v[126:129], v[138:141], v[10:13]
	s_add_u32 s50, s30, s40
	s_addc_u32 s51, s31, 0
	s_add_u32 m0, s44, 0xb000
	v_mfma_f32_16x16x32_f16 v[6:9], v[122:125], v[146:149], v[6:9]
	global_load_lds_dwordx4 v222, s[50:51]
	v_mfma_f32_16x16x32_f16 v[6:9], v[122:125], v[150:153], v[6:9]
	v_mfma_f32_16x16x32_f16 v[6:9], v[126:129], v[146:149], v[6:9]
	s_add_u32 s52, s34, s43
	s_addc_u32 s53, s35, 0
	s_add_u32 m0, s44, 0xf000
	v_mfma_f32_16x16x32_f16 v[2:5], v[122:125], v[154:157], v[2:5]
	global_load_lds_dwordx4 v223, s[52:53]
	v_mfma_f32_16x16x32_f16 v[2:5], v[122:125], v[158:161], v[2:5]
	v_mfma_f32_16x16x32_f16 v[2:5], v[126:129], v[154:157], v[2:5]
	s_waitcnt lgkmcnt(7)
	v_mfma_f32_16x16x32_f16 v[62:65], v[162:165], v[194:197], v[62:65]
	s_waitcnt lgkmcnt(6)
	v_mfma_f32_16x16x32_f16 v[62:65], v[162:165], v[198:201], v[62:65]
	v_mfma_f32_16x16x32_f16 v[62:65], v[166:169], v[194:197], v[62:65]
	s_waitcnt lgkmcnt(5)
	v_mfma_f32_16x16x32_f16 v[58:61], v[162:165], v[202:205], v[58:61]
	s_waitcnt lgkmcnt(4)
	v_mfma_f32_16x16x32_f16 v[58:61], v[162:165], v[206:209], v[58:61]
	v_mfma_f32_16x16x32_f16 v[58:61], v[166:169], v[202:205], v[58:61]
	s_waitcnt lgkmcnt(3)
	v_mfma_f32_16x16x32_f16 v[54:57], v[162:165], v[210:213], v[54:57]
	s_waitcnt lgkmcnt(2)
	v_mfma_f32_16x16x32_f16 v[54:57], v[162:165], v[214:217], v[54:57]
	v_mfma_f32_16x16x32_f16 v[54:57], v[166:169], v[210:213], v[54:57]
	s_waitcnt lgkmcnt(1)
	v_mfma_f32_16x16x32_f16 v[50:53], v[162:165], v[98:101], v[50:53]
	s_waitcnt lgkmcnt(0)
	v_mfma_f32_16x16x32_f16 v[50:53], v[162:165], v[218:221], v[50:53]
	v_mfma_f32_16x16x32_f16 v[50:53], v[166:169], v[98:101], v[50:53]
	v_mfma_f32_16x16x32_f16 v[46:49], v[170:173], v[194:197], v[46:49]
	v_mfma_f32_16x16x32_f16 v[46:49], v[170:173], v[198:201], v[46:49]
	v_mfma_f32_16x16x32_f16 v[46:49], v[174:177], v[194:197], v[46:49]
	v_mfma_f32_16x16x32_f16 v[42:45], v[170:173], v[202:205], v[42:45]
	v_mfma_f32_16x16x32_f16 v[42:45], v[170:173], v[206:209], v[42:45]
	v_mfma_f32_16x16x32_f16 v[42:45], v[174:177], v[202:205], v[42:45]
	v_mfma_f32_16x16x32_f16 v[38:41], v[170:173], v[210:213], v[38:41]
	v_mfma_f32_16x16x32_f16 v[38:41], v[170:173], v[214:217], v[38:41]
	v_mfma_f32_16x16x32_f16 v[38:41], v[174:177], v[210:213], v[38:41]
	v_mfma_f32_16x16x32_f16 v[34:37], v[170:173], v[98:101], v[34:37]
	v_mfma_f32_16x16x32_f16 v[34:37], v[170:173], v[218:221], v[34:37]
	v_mfma_f32_16x16x32_f16 v[34:37], v[174:177], v[98:101], v[34:37]
	v_mfma_f32_16x16x32_f16 v[30:33], v[178:181], v[194:197], v[30:33]
	v_mfma_f32_16x16x32_f16 v[30:33], v[178:181], v[198:201], v[30:33]
	v_mfma_f32_16x16x32_f16 v[30:33], v[182:185], v[194:197], v[30:33]
	v_mfma_f32_16x16x32_f16 v[26:29], v[178:181], v[202:205], v[26:29]
	v_mfma_f32_16x16x32_f16 v[26:29], v[178:181], v[206:209], v[26:29]
	v_mfma_f32_16x16x32_f16 v[26:29], v[182:185], v[202:205], v[26:29]
	v_mfma_f32_16x16x32_f16 v[22:25], v[178:181], v[210:213], v[22:25]
	v_mfma_f32_16x16x32_f16 v[22:25], v[178:181], v[214:217], v[22:25]
	v_mfma_f32_16x16x32_f16 v[22:25], v[182:185], v[210:213], v[22:25]
	v_mfma_f32_16x16x32_f16 v[18:21], v[178:181], v[98:101], v[18:21]
	v_mfma_f32_16x16x32_f16 v[18:21], v[178:181], v[218:221], v[18:21]
	v_mfma_f32_16x16x32_f16 v[18:21], v[182:185], v[98:101], v[18:21]
	v_mfma_f32_16x16x32_f16 v[14:17], v[186:189], v[194:197], v[14:17]
	v_mfma_f32_16x16x32_f16 v[14:17], v[186:189], v[198:201], v[14:17]
	v_mfma_f32_16x16x32_f16 v[14:17], v[190:193], v[194:197], v[14:17]
	v_mfma_f32_16x16x32_f16 v[10:13], v[186:189], v[202:205], v[10:13]
	v_mfma_f32_16x16x32_f16 v[10:13], v[186:189], v[206:209], v[10:13]
	v_mfma_f32_16x16x32_f16 v[10:13], v[190:193], v[202:205], v[10:13]
	v_mfma_f32_16x16x32_f16 v[6:9], v[186:189], v[210:213], v[6:9]
	v_mfma_f32_16x16x32_f16 v[6:9], v[186:189], v[214:217], v[6:9]
	v_mfma_f32_16x16x32_f16 v[6:9], v[190:193], v[210:213], v[6:9]
	v_mfma_f32_16x16x32_f16 v[2:5], v[186:189], v[98:101], v[2:5]
	v_mfma_f32_16x16x32_f16 v[2:5], v[186:189], v[218:221], v[2:5]
	v_mfma_f32_16x16x32_f16 v[2:5], v[190:193], v[98:101], v[2:5]
	s_branch .Lloop_k6

.LBB10_43:
	s_min_i32 s16, s15, 0x4400
	s_cmp_lt_i32 s14, s16
	s_cselect_b64 s[4:5], -1, 0
	s_and_b64 s[4:5], s[2:3], s[4:5]
	s_andn2_b64 vcc, exec, s[4:5]
	s_cbranch_vccnz .LBB10_319
	s_waitcnt lgkmcnt(0)
	s_load_dword s10, s[0:1], 0x48
	s_lshl_b32 s18, s18, 7
	v_lshrrev_b32_e32 v1, 1, v0
	v_mov_b32_e32 v65, 0
	v_and_b32_e32 v71, 15, v0
	v_bfe_u32 v70, v0, 4, 2
	v_and_b32_e32 v72, 64, v1
	v_lshlrev_b32_e32 v74, 7, v0
	v_and_b32_e32 v73, 7, v0
	s_waitcnt lgkmcnt(0)
	s_cmp_lt_i32 s10, 64
	v_mov_b32_e32 v64, v65
	v_mov_b32_e32 v63, v65
	v_mov_b32_e32 v62, v65
	v_mov_b32_e32 v61, v65
	v_mov_b32_e32 v60, v65
	v_mov_b32_e32 v59, v65
	v_mov_b32_e32 v58, v65
	v_mov_b32_e32 v57, v65
	v_mov_b32_e32 v56, v65
	v_mov_b32_e32 v55, v65
	v_mov_b32_e32 v54, v65
	v_mov_b32_e32 v53, v65
	v_mov_b32_e32 v52, v65
	v_mov_b32_e32 v51, v65
	v_mov_b32_e32 v50, v65
	v_mov_b32_e32 v49, v65
	v_mov_b32_e32 v48, v65
	v_mov_b32_e32 v47, v65
	v_mov_b32_e32 v46, v65
	v_mov_b32_e32 v45, v65
	v_mov_b32_e32 v44, v65
	v_mov_b32_e32 v43, v65
	v_mov_b32_e32 v42, v65
	v_mov_b32_e32 v41, v65
	v_mov_b32_e32 v40, v65
	v_mov_b32_e32 v39, v65
	v_mov_b32_e32 v38, v65
	v_mov_b32_e32 v37, v65
	v_mov_b32_e32 v36, v65
	v_mov_b32_e32 v35, v65
	v_mov_b32_e32 v34, v65
	v_mov_b32_e32 v33, v65
	v_mov_b32_e32 v32, v65
	v_mov_b32_e32 v31, v65
	v_mov_b32_e32 v30, v65
	v_mov_b32_e32 v29, v65
	v_mov_b32_e32 v28, v65
	v_mov_b32_e32 v27, v65
	v_mov_b32_e32 v26, v65
	v_mov_b32_e32 v25, v65
	v_mov_b32_e32 v24, v65
	v_mov_b32_e32 v23, v65
	v_mov_b32_e32 v22, v65
	v_mov_b32_e32 v21, v65
	v_mov_b32_e32 v20, v65
	v_mov_b32_e32 v19, v65
	v_mov_b32_e32 v18, v65
	v_mov_b32_e32 v17, v65
	v_mov_b32_e32 v16, v65
	v_mov_b32_e32 v15, v65
	v_mov_b32_e32 v14, v65
	v_mov_b32_e32 v13, v65
	v_mov_b32_e32 v12, v65
	v_mov_b32_e32 v11, v65
	v_mov_b32_e32 v10, v65
	v_mov_b32_e32 v9, v65
	v_mov_b32_e32 v8, v65
	v_mov_b32_e32 v7, v65
	v_mov_b32_e32 v6, v65
	v_mov_b32_e32 v5, v65
	v_mov_b32_e32 v4, v65
	v_mov_b32_e32 v3, v65
	v_mov_b32_e32 v2, v65
	s_cbranch_scc1 .LBB10_47
	s_load_dword s36, s[0:1], 0x10
	s_load_dwordx4 s[28:31], s[0:1], 0x0
	s_load_dwordx4 s[32:35], s[0:1], 0x30
	s_load_dwordx2 s[46:47], s[0:1], 0x40
	s_mov_b32 s37, s10
	s_lshr_b32 s45, s10, 6
	s_mul_i32 s48, s19, s45
	s_lshl_b32 s48, s48, 7
	v_lshrrev_b32_e32 v86, 6, v0
	v_lshlrev_b32_e32 v86, 10, v86
	v_lshrrev_b32_e32 v146, 3, v0
	v_readfirstlane_b32 s44, v86
	v_and_b32_e32 v147, 7, v0
	v_and_b32_e32 v86, 7, v146
	v_xor_b32_e32 v147, v147, v86
	v_lshlrev_b32_e32 v147, 4, v147
	s_waitcnt lgkmcnt(0)
	s_lshl_b32 s38, s36, 6
	s_lshl_b32 s39, s36, 7
	s_add_u32 s40, s38, s39
	s_lshl_b32 s41, s37, 6
	s_lshl_b32 s42, s37, 7
	s_add_u32 s43, s41, s42
	s_mul_i32 s54, s14, s36
	s_lshl_b32 s54, s54, 1
	s_add_u32 s54, s54, s48
	s_add_u32 s28, s28, s54
	s_addc_u32 s29, s29, 0
	s_add_u32 s30, s30, s54
	s_addc_u32 s31, s31, 0
	s_mul_i32 s54, s17, s46
	s_mul_i32 s55, s18, s37
	s_add_u32 s54, s54, s55
	s_lshl_b32 s54, s54, 1
	s_add_u32 s54, s54, s48
	s_add_u32 s32, s32, s54
	s_addc_u32 s33, s33, 0
	s_add_u32 s34, s34, s54
	s_addc_u32 s35, s35, 0
	s_lshl_b32 s54, s36, 1
	s_lshl_b32 s55, s37, 1
	v_mul_lo_u32 v86, v146, s54
	v_mul_lo_u32 v146, v146, s55
	v_add_u32_e32 v147, v147, v146
	v_sub_u32_e32 v146, v147, v146
	v_add_u32_e32 v146, v146, v86
	v_and_b32_e32 v86, 15, v0
	v_lshrrev_b32_e32 v82, 1, v0
	v_and_b32_e32 v82, 64, v82
	v_or_b32_e32 v82, v82, v86
	v_lshlrev_b32_e32 v82, 7, v82
	v_lshlrev_b32_e32 v83, 7, v0
	v_and_b32_e32 v83, 0x2780, v83
	v_bfe_u32 v84, v0, 4, 2
	v_and_b32_e32 v85, 7, v0
	v_xor_b32_e32 v84, v84, v85
	v_lshlrev_b32_e32 v84, 4, v84
	v_xor_b32_e32 v85, 64, v84
	v_add_u32_e32 v86, v82, v85
	v_add_u32_e32 v85, v83, v85
	v_add_u32_e32 v82, v82, v84
	v_add_u32_e32 v83, v83, v84
	v_mov_b32_e32 v84, v86
	s_mov_b64 s[50:51], s[28:29]
	s_mov_b32 m0, s44
	s_nop 0
	global_load_lds_dwordx4 v146, s[50:51]
	s_mov_b64 s[52:53], s[32:33]
	s_add_u32 m0, s44, 0x4000
	s_nop 0
	global_load_lds_dwordx4 v147, s[52:53]
	s_add_u32 s50, s28, s38
	s_addc_u32 s51, s29, 0
	s_add_u32 m0, s44, 0x1000
	s_nop 0
	global_load_lds_dwordx4 v146, s[50:51]
	s_add_u32 s52, s32, s41
	s_addc_u32 s53, s33, 0
	s_add_u32 m0, s44, 0x5000
	s_nop 0
	global_load_lds_dwordx4 v147, s[52:53]
	s_add_u32 s50, s28, s39
	s_addc_u32 s51, s29, 0
	s_add_u32 m0, s44, 0x2000
	s_nop 0
	global_load_lds_dwordx4 v146, s[50:51]
	s_add_u32 s52, s32, s42
	s_addc_u32 s53, s33, 0
	s_add_u32 m0, s44, 0x6000
	s_nop 0
	global_load_lds_dwordx4 v147, s[52:53]
	s_add_u32 s50, s28, s40
	s_addc_u32 s51, s29, 0
	s_add_u32 m0, s44, 0x3000
	s_nop 0
	global_load_lds_dwordx4 v146, s[50:51]
	s_add_u32 s52, s32, s43
	s_addc_u32 s53, s33, 0
	s_add_u32 m0, s44, 0x7000
	s_nop 0
	global_load_lds_dwordx4 v147, s[52:53]
.Lloop_k10:
	s_waitcnt vmcnt(0)
	s_barrier
	ds_read_b128 v[86:89], v82
	ds_read_b128 v[90:93], v82 offset:2048
	ds_read_b128 v[94:97], v82 offset:4096
	ds_read_b128 v[98:101], v82 offset:6144
	ds_read_b128 v[102:105], v83 offset:16384
	ds_read_b128 v[106:109], v83 offset:18432
	s_waitcnt lgkmcnt(1)
	v_mfma_f32_16x16x32_f16 v[62:65], v[86:89], v[102:105], v[62:65]
	ds_read_b128 v[110:113], v83 offset:20480
	ds_read_b128 v[114:117], v83 offset:22528
	s_waitcnt lgkmcnt(2)
	v_mfma_f32_16x16x32_f16 v[58:61], v[86:89], v[106:109], v[58:61]
	ds_read_b128 v[118:121], v84
	ds_read_b128 v[122:125], v84 offset:2048
	s_waitcnt lgkmcnt(3)
	v_mfma_f32_16x16x32_f16 v[54:57], v[86:89], v[110:113], v[54:57]
	ds_read_b128 v[126:129], v84 offset:4096
	ds_read_b128 v[130:133], v84 offset:6144
	s_waitcnt lgkmcnt(4)
	v_mfma_f32_16x16x32_f16 v[50:53], v[86:89], v[114:117], v[50:53]
	ds_read_b128 v[86:89], v85 offset:16384
	ds_read_b128 v[134:137], v85 offset:18432
	v_mfma_f32_16x16x32_f16 v[46:49], v[90:93], v[102:105], v[46:49]
	ds_read_b128 v[138:141], v85 offset:20480
	ds_read_b128 v[142:145], v85 offset:22528
	v_mfma_f32_16x16x32_f16 v[42:45], v[90:93], v[106:109], v[42:45]
	v_mfma_f32_16x16x32_f16 v[38:41], v[90:93], v[110:113], v[38:41]
	v_mfma_f32_16x16x32_f16 v[34:37], v[90:93], v[114:117], v[34:37]
	s_waitcnt lgkmcnt(0)
	s_barrier
	s_add_i32 s45, s45, -1
	s_cmp_eq_u32 s45, 0
	s_cbranch_scc1 .Llast_k10
	s_add_u32 s28, s28, 0x80
	s_addc_u32 s29, s29, 0
	s_add_u32 s32, s32, 0x80
	s_addc_u32 s33, s33, 0
	s_mov_b64 s[50:51], s[28:29]
	s_mov_b32 m0, s44
	v_mfma_f32_16x16x32_f16 v[30:33], v[94:97], v[102:105], v[30:33]
	global_load_lds_dwordx4 v146, s[50:51]
	v_mfma_f32_16x16x32_f16 v[26:29], v[94:97], v[106:109], v[26:29]
	v_mfma_f32_16x16x32_f16 v[22:25], v[94:97], v[110:113], v[22:25]
	s_mov_b64 s[52:53], s[32:33]
	s_add_u32 m0, s44, 0x4000
	v_mfma_f32_16x16x32_f16 v[18:21], v[94:97], v[114:117], v[18:21]
	global_load_lds_dwordx4 v147, s[52:53]
	v_mfma_f32_16x16x32_f16 v[14:17], v[98:101], v[102:105], v[14:17]
	v_mfma_f32_16x16x32_f16 v[10:13], v[98:101], v[106:109], v[10:13]
	s_add_u32 s50, s28, s38
	s_addc_u32 s51, s29, 0
	s_add_u32 m0, s44, 0x1000
	v_mfma_f32_16x16x32_f16 v[6:9], v[98:101], v[110:113], v[6:9]
	global_load_lds_dwordx4 v146, s[50:51]
	v_mfma_f32_16x16x32_f16 v[2:5], v[98:101], v[114:117], v[2:5]
	s_waitcnt lgkmcnt(3)
	v_mfma_f32_16x16x32_f16 v[62:65], v[118:121], v[86:89], v[62:65]
	s_add_u32 s52, s32, s41
	s_addc_u32 s53, s33, 0
	s_add_u32 m0, s44, 0x5000
	s_waitcnt lgkmcnt(2)
	v_mfma_f32_16x16x32_f16 v[58:61], v[118:121], v[134:137], v[58:61]
	global_load_lds_dwordx4 v147, s[52:53]
	s_waitcnt lgkmcnt(1)
	v_mfma_f32_16x16x32_f16 v[54:57], v[118:121], v[138:141], v[54:57]
	s_waitcnt lgkmcnt(0)
	v_mfma_f32_16x16x32_f16 v[50:53], v[118:121], v[142:145], v[50:53]
	s_add_u32 s50, s28, s39
	s_addc_u32 s51, s29, 0
	s_add_u32 m0, s44, 0x2000
	v_mfma_f32_16x16x32_f16 v[46:49], v[122:125], v[86:89], v[46:49]
	global_load_lds_dwordx4 v146, s[50:51]
	v_mfma_f32_16x16x32_f16 v[42:45], v[122:125], v[134:137], v[42:45]
	v_mfma_f32_16x16x32_f16 v[38:41], v[122:125], v[138:141], v[38:41]
	s_add_u32 s52, s32, s42
	s_addc_u32 s53, s33, 0
	s_add_u32 m0, s44, 0x6000
	v_mfma_f32_16x16x32_f16 v[34:37], v[122:125], v[142:145], v[34:37]
	global_load_lds_dwordx4 v147, s[52:53]
	v_mfma_f32_16x16x32_f16 v[30:33], v[126:129], v[86:89], v[30:33]
	v_mfma_f32_16x16x32_f16 v[26:29], v[126:129], v[134:137], v[26:29]
	s_add_u32 s50, s28, s40
	s_addc_u32 s51, s29, 0
	s_add_u32 m0, s44, 0x3000
	v_mfma_f32_16x16x32_f16 v[22:25], v[126:129], v[138:141], v[22:25]
	global_load_lds_dwordx4 v146, s[50:51]
	v_mfma_f32_16x16x32_f16 v[18:21], v[126:129], v[142:145], v[18:21]
	v_mfma_f32_16x16x32_f16 v[14:17], v[130:133], v[86:89], v[14:17]
	s_add_u32 s52, s32, s43
	s_addc_u32 s53, s33, 0
	s_add_u32 m0, s44, 0x7000
	v_mfma_f32_16x16x32_f16 v[10:13], v[130:133], v[134:137], v[10:13]
	global_load_lds_dwordx4 v147, s[52:53]
	v_mfma_f32_16x16x32_f16 v[6:9], v[130:133], v[138:141], v[6:9]
	v_mfma_f32_16x16x32_f16 v[2:5], v[130:133], v[142:145], v[2:5]
	s_branch .Lloop_k10
.Llast_k10:
	v_mfma_f32_16x16x32_f16 v[30:33], v[94:97], v[102:105], v[30:33]
	v_mfma_f32_16x16x32_f16 v[26:29], v[94:97], v[106:109], v[26:29]
	v_mfma_f32_16x16x32_f16 v[22:25], v[94:97], v[110:113], v[22:25]
	v_mfma_f32_16x16x32_f16 v[18:21], v[94:97], v[114:117], v[18:21]
	v_mfma_f32_16x16x32_f16 v[14:17], v[98:101], v[102:105], v[14:17]
	v_mfma_f32_16x16x32_f16 v[10:13], v[98:101], v[106:109], v[10:13]
	v_mfma_f32_16x16x32_f16 v[6:9], v[98:101], v[110:113], v[6:9]
	v_mfma_f32_16x16x32_f16 v[2:5], v[98:101], v[114:117], v[2:5]
	s_waitcnt lgkmcnt(3)
	v_mfma_f32_16x16x32_f16 v[62:65], v[118:121], v[86:89], v[62:65]
	s_waitcnt lgkmcnt(2)
	v_mfma_f32_16x16x32_f16 v[58:61], v[118:121], v[134:137], v[58:61]
	s_waitcnt lgkmcnt(1)
	v_mfma_f32_16x16x32_f16 v[54:57], v[118:121], v[138:141], v[54:57]
	s_waitcnt lgkmcnt(0)
	v_mfma_f32_16x16x32_f16 v[50:53], v[118:121], v[142:145], v[50:53]
	v_mfma_f32_16x16x32_f16 v[46:49], v[122:125], v[86:89], v[46:49]
	v_mfma_f32_16x16x32_f16 v[42:45], v[122:125], v[134:137], v[42:45]
	v_mfma_f32_16x16x32_f16 v[38:41], v[122:125], v[138:141], v[38:41]
	v_mfma_f32_16x16x32_f16 v[34:37], v[122:125], v[142:145], v[34:37]
	v_mfma_f32_16x16x32_f16 v[30:33], v[126:129], v[86:89], v[30:33]
	v_mfma_f32_16x16x32_f16 v[26:29], v[126:129], v[134:137], v[26:29]
	v_mfma_f32_16x16x32_f16 v[22:25], v[126:129], v[138:141], v[22:25]
	v_mfma_f32_16x16x32_f16 v[18:21], v[126:129], v[142:145], v[18:21]
	v_mfma_f32_16x16x32_f16 v[14:17], v[130:133], v[86:89], v[14:17]
	v_mfma_f32_16x16x32_f16 v[10:13], v[130:133], v[134:137], v[10:13]
	v_mfma_f32_16x16x32_f16 v[6:9], v[130:133], v[138:141], v[6:9]
	v_mfma_f32_16x16x32_f16 v[2:5], v[130:133], v[142:145], v[2:5]

	.amdhsa_kernel _Z13gemm64_kernelILi1ELi2ELb1ELi1EEv2GP
		.amdhsa_group_segment_fixed_size 32768
		.amdhsa_private_segment_fixed_size 0
		.amdhsa_kernarg_size 440
		.amdhsa_user_sgpr_count 2
		.amdhsa_user_sgpr_dispatch_ptr 0
		.amdhsa_user_sgpr_queue_ptr 0
		.amdhsa_user_sgpr_kernarg_segment_ptr 1
		.amdhsa_user_sgpr_dispatch_id 0
		.amdhsa_user_sgpr_kernarg_preload_length 0
		.amdhsa_user_sgpr_kernarg_preload_offset 0
		.amdhsa_user_sgpr_private_segment_size 0
		.amdhsa_uses_dynamic_stack 0
		.amdhsa_enable_private_segment 0
		.amdhsa_system_sgpr_workgroup_id_x 1
		.amdhsa_system_sgpr_workgroup_id_y 1
		.amdhsa_system_sgpr_workgroup_id_z 0
		.amdhsa_system_sgpr_workgroup_info 0
		.amdhsa_system_vgpr_workitem_id 0
		.amdhsa_next_free_vgpr 148
		.amdhsa_next_free_sgpr 96
		.amdhsa_accum_offset 148
		.amdhsa_reserve_vcc 1
		.amdhsa_float_round_mode_32 0
		.amdhsa_float_round_mode_16_64 0
		.amdhsa_float_denorm_mode_32 3
		.amdhsa_float_denorm_mode_16_64 3
		.amdhsa_dx10_clamp 1
		.amdhsa_ieee_mode 1
		.amdhsa_fp16_overflow 0
		.amdhsa_tg_split 0
		.amdhsa_exception_fp_ieee_invalid_op 0
		.amdhsa_exception_fp_denorm_src 0
		.amdhsa_exception_fp_ieee_div_zero 0
		.amdhsa_exception_fp_ieee_overflow 0
		.amdhsa_exception_fp_ieee_underflow 0
		.amdhsa_exception_fp_ieee_inexact 0
		.amdhsa_exception_int_div_zero 0
	.end_amdhsa_kernel

.LBB13_43:
	s_min_i32 s17, s15, 0x4400
	s_cmp_lt_i32 s14, s17
	s_cselect_b64 s[4:5], -1, 0
	s_and_b64 s[4:5], s[2:3], s[4:5]
	s_andn2_b64 vcc, exec, s[4:5]
	s_cbranch_vccnz .LBB13_111
	s_waitcnt lgkmcnt(0)
	s_load_dword s8, s[0:1], 0x48
	s_lshl_b32 s18, s18, 7
	v_lshrrev_b32_e32 v1, 1, v0
	v_mov_b32_e32 v65, 0
	v_and_b32_e32 v71, 15, v0
	v_bfe_u32 v70, v0, 4, 2
	v_and_b32_e32 v73, 64, v1
	v_lshlrev_b32_e32 v72, 7, v0
	s_waitcnt lgkmcnt(0)
	s_cmp_lt_i32 s8, 64
	v_mov_b32_e32 v64, v65
	v_mov_b32_e32 v63, v65
	v_mov_b32_e32 v62, v65
	v_mov_b32_e32 v61, v65
	v_mov_b32_e32 v60, v65
	v_mov_b32_e32 v59, v65
	v_mov_b32_e32 v58, v65
	v_mov_b32_e32 v57, v65
	v_mov_b32_e32 v56, v65
	v_mov_b32_e32 v55, v65
	v_mov_b32_e32 v54, v65
	v_mov_b32_e32 v53, v65
	v_mov_b32_e32 v52, v65
	v_mov_b32_e32 v51, v65
	v_mov_b32_e32 v50, v65
	v_mov_b32_e32 v49, v65
	v_mov_b32_e32 v48, v65
	v_mov_b32_e32 v47, v65
	v_mov_b32_e32 v46, v65
	v_mov_b32_e32 v45, v65
	v_mov_b32_e32 v44, v65
	v_mov_b32_e32 v43, v65
	v_mov_b32_e32 v42, v65
	v_mov_b32_e32 v41, v65
	v_mov_b32_e32 v40, v65
	v_mov_b32_e32 v39, v65
	v_mov_b32_e32 v38, v65
	v_mov_b32_e32 v37, v65
	v_mov_b32_e32 v36, v65
	v_mov_b32_e32 v35, v65
	v_mov_b32_e32 v34, v65
	v_mov_b32_e32 v33, v65
	v_mov_b32_e32 v32, v65
	v_mov_b32_e32 v31, v65
	v_mov_b32_e32 v30, v65
	v_mov_b32_e32 v29, v65
	v_mov_b32_e32 v28, v65
	v_mov_b32_e32 v27, v65
	v_mov_b32_e32 v26, v65
	v_mov_b32_e32 v25, v65
	v_mov_b32_e32 v24, v65
	v_mov_b32_e32 v23, v65
	v_mov_b32_e32 v22, v65
	v_mov_b32_e32 v21, v65
	v_mov_b32_e32 v20, v65
	v_mov_b32_e32 v19, v65
	v_mov_b32_e32 v18, v65
	v_mov_b32_e32 v17, v65
	v_mov_b32_e32 v16, v65
	v_mov_b32_e32 v15, v65
	v_mov_b32_e32 v14, v65
	v_mov_b32_e32 v13, v65
	v_mov_b32_e32 v12, v65
	v_mov_b32_e32 v11, v65
	v_mov_b32_e32 v10, v65
	v_mov_b32_e32 v9, v65
	v_mov_b32_e32 v8, v65
	v_mov_b32_e32 v7, v65
	v_mov_b32_e32 v6, v65
	v_mov_b32_e32 v5, v65
	v_mov_b32_e32 v4, v65
	v_mov_b32_e32 v3, v65
	v_mov_b32_e32 v2, v65
	s_cbranch_scc1 .LBB13_47
	s_load_dword s36, s[0:1], 0x10
	s_load_dwordx4 s[28:31], s[0:1], 0x0
	s_load_dwordx4 s[32:35], s[0:1], 0x30
	s_load_dwordx2 s[46:47], s[0:1], 0x40
	s_mov_b32 s37, s8
	s_lshr_b32 s45, s8, 6
	s_mul_i32 s48, s19, s45
	s_lshl_b32 s48, s48, 7
	v_lshrrev_b32_e32 v86, 6, v0
	v_lshlrev_b32_e32 v86, 10, v86
	v_lshrrev_b32_e32 v118, 3, v0
	v_readfirstlane_b32 s44, v86
	v_and_b32_e32 v119, 7, v0
	v_and_b32_e32 v86, 7, v118
	v_xor_b32_e32 v119, v119, v86
	v_lshlrev_b32_e32 v119, 4, v119
	s_waitcnt lgkmcnt(0)
	s_lshl_b32 s38, s36, 6
	s_lshl_b32 s39, s36, 7
	s_add_u32 s40, s38, s39
	s_lshl_b32 s41, s37, 6
	s_lshl_b32 s42, s37, 7
	s_add_u32 s43, s41, s42
	s_mul_i32 s54, s14, s36
	s_lshl_b32 s54, s54, 1
	s_add_u32 s54, s54, s48
	s_add_u32 s28, s28, s54
	s_addc_u32 s29, s29, 0
	s_add_u32 s30, s30, s54
	s_addc_u32 s31, s31, 0
	s_mul_i32 s54, s16, s46
	s_mul_i32 s55, s18, s37
	s_add_u32 s54, s54, s55
	s_lshl_b32 s54, s54, 1
	s_add_u32 s54, s54, s48
	s_add_u32 s32, s32, s54
	s_addc_u32 s33, s33, 0
	s_add_u32 s34, s34, s54
	s_addc_u32 s35, s35, 0
	s_lshl_b32 s54, s36, 1
	s_lshl_b32 s55, s37, 1
	v_mul_lo_u32 v86, v118, s54
	v_mul_lo_u32 v118, v118, s55
	v_add_u32_e32 v119, v119, v118
	v_sub_u32_e32 v118, v119, v118
	v_add_u32_e32 v118, v118, v86
	v_and_b32_e32 v86, 15, v0
	v_lshrrev_b32_e32 v81, 1, v0
	v_and_b32_e32 v81, 64, v81
	v_or_b32_e32 v81, v81, v86
	v_lshlrev_b32_e32 v81, 7, v81
	v_lshlrev_b32_e32 v82, 7, v0
	v_and_b32_e32 v82, 0x2780, v82
	v_bfe_u32 v83, v0, 4, 2
	v_and_b32_e32 v84, 7, v0
	v_xor_b32_e32 v83, v83, v84
	v_lshlrev_b32_e32 v83, 4, v83
	v_xor_b32_e32 v84, 64, v83
	v_add_u32_e32 v86, v81, v84
	v_add_u32_e32 v84, v82, v84
	v_add_u32_e32 v81, v81, v83
	v_add_u32_e32 v82, v82, v83
	v_mov_b32_e32 v83, v86
	s_mov_b64 s[50:51], s[28:29]
	s_mov_b32 m0, s44
	s_nop 0
	global_load_lds_dwordx4 v118, s[50:51]
	s_mov_b64 s[52:53], s[32:33]
	s_add_u32 m0, s44, 0x4000
	s_nop 0
	global_load_lds_dwordx4 v119, s[52:53]
	s_add_u32 s50, s28, s38
	s_addc_u32 s51, s29, 0
	s_add_u32 m0, s44, 0x1000
	s_nop 0
	global_load_lds_dwordx4 v118, s[50:51]
	s_add_u32 s52, s32, s41
	s_addc_u32 s53, s33, 0
	s_add_u32 m0, s44, 0x5000
	s_nop 0
	global_load_lds_dwordx4 v119, s[52:53]
	s_add_u32 s50, s28, s39
	s_addc_u32 s51, s29, 0
	s_add_u32 m0, s44, 0x2000
	s_nop 0
	global_load_lds_dwordx4 v118, s[50:51]
	s_add_u32 s52, s32, s42
	s_addc_u32 s53, s33, 0
	s_add_u32 m0, s44, 0x6000
	s_nop 0
	global_load_lds_dwordx4 v119, s[52:53]
	s_add_u32 s50, s28, s40
	s_addc_u32 s51, s29, 0
	s_add_u32 m0, s44, 0x3000
	s_nop 0
	global_load_lds_dwordx4 v118, s[50:51]
	s_add_u32 s52, s32, s43
	s_addc_u32 s53, s33, 0
	s_add_u32 m0, s44, 0x7000
	s_nop 0
	global_load_lds_dwordx4 v119, s[52:53]
.Lloop_k13:
	s_waitcnt vmcnt(0)
	s_barrier
	ds_read_b128 v[86:89], v81
	ds_read_b128 v[90:93], v81 offset:2048
	ds_read_b128 v[94:97], v81 offset:4096
	ds_read_b128 v[98:101], v81 offset:6144
	ds_read_b128 v[102:105], v82 offset:16384
	ds_read_b128 v[106:109], v82 offset:18432
	s_waitcnt lgkmcnt(1)
	v_mfma_f32_16x16x32_f16 v[62:65], v[86:89], v[102:105], v[62:65]
	ds_read_b128 v[110:113], v82 offset:20480
	ds_read_b128 v[114:117], v82 offset:22528
	s_waitcnt lgkmcnt(2)
	v_mfma_f32_16x16x32_f16 v[58:61], v[86:89], v[106:109], v[58:61]
	s_waitcnt lgkmcnt(1)
	v_mfma_f32_16x16x32_f16 v[54:57], v[86:89], v[110:113], v[54:57]
	s_waitcnt lgkmcnt(0)
	v_mfma_f32_16x16x32_f16 v[50:53], v[86:89], v[114:117], v[50:53]
	ds_read_b128 v[86:89], v83
	v_mfma_f32_16x16x32_f16 v[46:49], v[90:93], v[102:105], v[46:49]
	v_mfma_f32_16x16x32_f16 v[42:45], v[90:93], v[106:109], v[42:45]
	v_mfma_f32_16x16x32_f16 v[38:41], v[90:93], v[110:113], v[38:41]
	v_mfma_f32_16x16x32_f16 v[34:37], v[90:93], v[114:117], v[34:37]
	ds_read_b128 v[90:93], v83 offset:2048
	v_mfma_f32_16x16x32_f16 v[30:33], v[94:97], v[102:105], v[30:33]
	v_mfma_f32_16x16x32_f16 v[26:29], v[94:97], v[106:109], v[26:29]
	v_mfma_f32_16x16x32_f16 v[22:25], v[94:97], v[110:113], v[22:25]
	v_mfma_f32_16x16x32_f16 v[18:21], v[94:97], v[114:117], v[18:21]
	ds_read_b128 v[94:97], v83 offset:4096
	v_mfma_f32_16x16x32_f16 v[14:17], v[98:101], v[102:105], v[14:17]
	ds_read_b128 v[102:105], v84 offset:16384
	v_mfma_f32_16x16x32_f16 v[10:13], v[98:101], v[106:109], v[10:13]
	ds_read_b128 v[106:109], v84 offset:18432
	v_mfma_f32_16x16x32_f16 v[6:9], v[98:101], v[110:113], v[6:9]
	ds_read_b128 v[110:113], v84 offset:20480
	v_mfma_f32_16x16x32_f16 v[2:5], v[98:101], v[114:117], v[2:5]
	ds_read_b128 v[98:101], v83 offset:6144
	ds_read_b128 v[114:117], v84 offset:22528
	s_waitcnt lgkmcnt(4)
	v_mfma_f32_16x16x32_f16 v[62:65], v[86:89], v[102:105], v[62:65]
	s_waitcnt lgkmcnt(3)
	v_mfma_f32_16x16x32_f16 v[58:61], v[86:89], v[106:109], v[58:61]
	s_waitcnt lgkmcnt(0)
	s_barrier
	s_add_i32 s45, s45, -1
	s_cmp_eq_u32 s45, 0
	s_cbranch_scc1 .Llast_k13
	s_add_u32 s28, s28, 0x80
	s_addc_u32 s29, s29, 0
	s_add_u32 s32, s32, 0x80
	s_addc_u32 s33, s33, 0
	s_mov_b64 s[50:51], s[28:29]
	s_mov_b32 m0, s44
	s_waitcnt lgkmcnt(2)
	v_mfma_f32_16x16x32_f16 v[54:57], v[86:89], v[110:113], v[54:57]
	global_load_lds_dwordx4 v118, s[50:51]
	s_mov_b64 s[52:53], s[32:33]
	s_add_u32 m0, s44, 0x4000
	s_waitcnt lgkmcnt(0)
	v_mfma_f32_16x16x32_f16 v[50:53], v[86:89], v[114:117], v[50:53]
	global_load_lds_dwordx4 v119, s[52:53]
	s_add_u32 s50, s28, s38
	s_addc_u32 s51, s29, 0
	s_add_u32 m0, s44, 0x1000
	v_mfma_f32_16x16x32_f16 v[46:49], v[90:93], v[102:105], v[46:49]
	global_load_lds_dwordx4 v118, s[50:51]
	s_add_u32 s52, s32, s41
	s_addc_u32 s53, s33, 0
	s_add_u32 m0, s44, 0x5000
	v_mfma_f32_16x16x32_f16 v[42:45], v[90:93], v[106:109], v[42:45]
	global_load_lds_dwordx4 v119, s[52:53]
	s_add_u32 s50, s28, s39
	s_addc_u32 s51, s29, 0
	s_add_u32 m0, s44, 0x2000
	v_mfma_f32_16x16x32_f16 v[38:41], v[90:93], v[110:113], v[38:41]
	global_load_lds_dwordx4 v118, s[50:51]
	s_add_u32 s52, s32, s42
	s_addc_u32 s53, s33, 0
	s_add_u32 m0, s44, 0x6000
	v_mfma_f32_16x16x32_f16 v[34:37], v[90:93], v[114:117], v[34:37]
	global_load_lds_dwordx4 v119, s[52:53]
	s_add_u32 s50, s28, s40
	s_addc_u32 s51, s29, 0
	s_add_u32 m0, s44, 0x3000
	v_mfma_f32_16x16x32_f16 v[30:33], v[94:97], v[102:105], v[30:33]
	global_load_lds_dwordx4 v118, s[50:51]
	s_add_u32 s52, s32, s43
	s_addc_u32 s53, s33, 0
	s_add_u32 m0, s44, 0x7000
	v_mfma_f32_16x16x32_f16 v[26:29], v[94:97], v[106:109], v[26:29]
	global_load_lds_dwordx4 v119, s[52:53]
	v_mfma_f32_16x16x32_f16 v[22:25], v[94:97], v[110:113], v[22:25]
	v_mfma_f32_16x16x32_f16 v[18:21], v[94:97], v[114:117], v[18:21]
	v_mfma_f32_16x16x32_f16 v[14:17], v[98:101], v[102:105], v[14:17]
	v_mfma_f32_16x16x32_f16 v[10:13], v[98:101], v[106:109], v[10:13]
	v_mfma_f32_16x16x32_f16 v[6:9], v[98:101], v[110:113], v[6:9]
	v_mfma_f32_16x16x32_f16 v[2:5], v[98:101], v[114:117], v[2:5]
	s_branch .Lloop_k13
.Llast_k13:
	s_waitcnt lgkmcnt(2)
	v_mfma_f32_16x16x32_f16 v[54:57], v[86:89], v[110:113], v[54:57]
	s_waitcnt lgkmcnt(0)
	v_mfma_f32_16x16x32_f16 v[50:53], v[86:89], v[114:117], v[50:53]
	v_mfma_f32_16x16x32_f16 v[46:49], v[90:93], v[102:105], v[46:49]
	v_mfma_f32_16x16x32_f16 v[42:45], v[90:93], v[106:109], v[42:45]
	v_mfma_f32_16x16x32_f16 v[38:41], v[90:93], v[110:113], v[38:41]
	v_mfma_f32_16x16x32_f16 v[34:37], v[90:93], v[114:117], v[34:37]
	v_mfma_f32_16x16x32_f16 v[30:33], v[94:97], v[102:105], v[30:33]
	v_mfma_f32_16x16x32_f16 v[26:29], v[94:97], v[106:109], v[26:29]
	v_mfma_f32_16x16x32_f16 v[22:25], v[94:97], v[110:113], v[22:25]
	v_mfma_f32_16x16x32_f16 v[18:21], v[94:97], v[114:117], v[18:21]
	v_mfma_f32_16x16x32_f16 v[14:17], v[98:101], v[102:105], v[14:17]
	v_mfma_f32_16x16x32_f16 v[10:13], v[98:101], v[106:109], v[10:13]
	v_mfma_f32_16x16x32_f16 v[6:9], v[98:101], v[110:113], v[6:9]
	v_mfma_f32_16x16x32_f16 v[2:5], v[98:101], v[114:117], v[2:5]

	.amdhsa_kernel _Z13gemm64_kernelILi1ELi3ELb1ELi1EEv2GP
		.amdhsa_group_segment_fixed_size 32768
		.amdhsa_private_segment_fixed_size 0
		.amdhsa_kernarg_size 440
		.amdhsa_user_sgpr_count 2
		.amdhsa_user_sgpr_dispatch_ptr 0
		.amdhsa_user_sgpr_queue_ptr 0
		.amdhsa_user_sgpr_kernarg_segment_ptr 1
		.amdhsa_user_sgpr_dispatch_id 0
		.amdhsa_user_sgpr_kernarg_preload_length 0
		.amdhsa_user_sgpr_kernarg_preload_offset 0
		.amdhsa_user_sgpr_private_segment_size 0
		.amdhsa_uses_dynamic_stack 0
		.amdhsa_enable_private_segment 0
		.amdhsa_system_sgpr_workgroup_id_x 1
		.amdhsa_system_sgpr_workgroup_id_y 1
		.amdhsa_system_sgpr_workgroup_id_z 0
		.amdhsa_system_sgpr_workgroup_info 0
		.amdhsa_system_vgpr_workitem_id 0
		.amdhsa_next_free_vgpr 120
		.amdhsa_next_free_sgpr 96
		.amdhsa_accum_offset 120
		.amdhsa_reserve_vcc 1
		.amdhsa_float_round_mode_32 0
		.amdhsa_float_round_mode_16_64 0
		.amdhsa_float_denorm_mode_32 3
		.amdhsa_float_denorm_mode_16_64 3
		.amdhsa_dx10_clamp 1
		.amdhsa_ieee_mode 1
		.amdhsa_fp16_overflow 0
		.amdhsa_tg_split 0
		.amdhsa_exception_fp_ieee_invalid_op 0
		.amdhsa_exception_fp_denorm_src 0
		.amdhsa_exception_fp_ieee_div_zero 0
		.amdhsa_exception_fp_ieee_overflow 0
		.amdhsa_exception_fp_ieee_underflow 0
		.amdhsa_exception_fp_ieee_inexact 0
		.amdhsa_exception_int_div_zero 0
	.end_amdhsa_kernel

amdhsa.kernels:
  - .agpr_count:     0
    .args:
      - .actual_access:  read_only
        .address_space:  global
        .offset:         0
        .size:           8
        .value_kind:     global_buffer
      - .actual_access:  read_only
        .address_space:  global
        .offset:         8
        .size:           8
        .value_kind:     global_buffer
      - .actual_access:  read_only
        .address_space:  global
        .offset:         16
        .size:           8
        .value_kind:     global_buffer
      - .actual_access:  read_only
        .address_space:  global
        .offset:         24
        .size:           8
        .value_kind:     global_buffer
      - .actual_access:  read_only
        .address_space:  global
        .offset:         32
        .size:           8
        .value_kind:     global_buffer
      - .actual_access:  read_only
        .address_space:  global
        .offset:         40
        .size:           8
        .value_kind:     global_buffer
      - .actual_access:  read_only
        .address_space:  global
        .offset:         48
        .size:           8
        .value_kind:     global_buffer
      - .actual_access:  read_only
        .address_space:  global
        .offset:         56
        .size:           8
        .value_kind:     global_buffer
      - .actual_access:  read_only
        .address_space:  global
        .offset:         64
        .size:           8
        .value_kind:     global_buffer
      - .actual_access:  write_only
        .address_space:  global
        .offset:         72
        .size:           8
        .value_kind:     global_buffer
      - .actual_access:  write_only
        .address_space:  global
        .offset:         80
        .size:           8
        .value_kind:     global_buffer
      - .actual_access:  write_only
        .address_space:  global
        .offset:         88
        .size:           8
        .value_kind:     global_buffer
      - .actual_access:  write_only
        .address_space:  global
        .offset:         96
        .size:           8
        .value_kind:     global_buffer
    .group_segment_fixed_size: 0
    .kernarg_segment_align: 8
    .kernarg_segment_size: 104
    .language:       OpenCL C
    .language_version:
      - 2
      - 0
    .max_flat_workgroup_size: 256
    .name:           _Z14scatter_kernelPKfS0_PKiS2_S2_S2_S0_S0_S0_PDF16_S3_PfPi
    .private_segment_fixed_size: 0
    .sgpr_count:     31
    .sgpr_spill_count: 0
    .symbol:         _Z14scatter_kernelPKfS0_PKiS2_S2_S2_S0_S0_S0_PDF16_S3_PfPi.kd
    .uniform_work_group_size: 1
    .uses_dynamic_stack: false
    .vgpr_count:     42
    .vgpr_spill_count: 0
    .wavefront_size: 64
  - .agpr_count:     144
    .args:
      - .actual_access:  read_only
        .address_space:  global
        .offset:         0
        .size:           8
        .value_kind:     global_buffer
      - .actual_access:  read_only
        .address_space:  global
        .offset:         8
        .size:           8
        .value_kind:     global_buffer
      - .actual_access:  read_only
        .address_space:  global
        .offset:         16
        .size:           8
        .value_kind:     global_buffer
      - .actual_access:  read_only
        .address_space:  global
        .offset:         24
        .size:           8
        .value_kind:     global_buffer
      - .actual_access:  read_only
        .address_space:  global
        .offset:         32
        .size:           8
        .value_kind:     global_buffer
      - .actual_access:  read_only
        .address_space:  global
        .offset:         40
        .size:           8
        .value_kind:     global_buffer
      - .actual_access:  write_only
        .address_space:  global
        .offset:         48
        .size:           8
        .value_kind:     global_buffer
      - .actual_access:  write_only
        .address_space:  global
        .offset:         56
        .size:           8
        .value_kind:     global_buffer
    .group_segment_fixed_size: 16384
    .kernarg_segment_align: 8
    .kernarg_segment_size: 64
    .language:       OpenCL C
    .language_version:
      - 2
      - 0
    .max_flat_workgroup_size: 128
    .name:           _Z10attn_naivePKDF16_S0_S0_S0_S0_S0_PDF16_S1_
    .private_segment_fixed_size: 0
    .sgpr_count:     28
    .sgpr_spill_count: 0
    .symbol:         _Z10attn_naivePKDF16_S0_S0_S0_S0_S0_PDF16_S1_.kd
    .uniform_work_group_size: 1
    .uses_dynamic_stack: false
    .vgpr_count:     400
    .vgpr_spill_count: 0
    .wavefront_size: 64
  - .agpr_count:     0
    .args:
      - .actual_access:  read_only
        .address_space:  global
        .offset:         0
        .size:           8
        .value_kind:     global_buffer
      - .actual_access:  read_only
        .address_space:  global
        .offset:         8
        .size:           8
        .value_kind:     global_buffer
      - .actual_access:  read_only
        .address_space:  global
        .offset:         16
        .size:           8
        .value_kind:     global_buffer
      - .actual_access:  read_only
        .address_space:  global
        .offset:         24
        .size:           8
        .value_kind:     global_buffer
      - .actual_access:  read_only
        .address_space:  global
        .offset:         32
        .size:           8
        .value_kind:     global_buffer
      - .actual_access:  read_only
        .address_space:  global
        .offset:         40
        .size:           8
        .value_kind:     global_buffer
      - .actual_access:  write_only
        .address_space:  global
        .offset:         48
        .size:           8
        .value_kind:     global_buffer
      - .actual_access:  write_only
        .address_space:  global
        .offset:         56
        .size:           8
        .value_kind:     global_buffer
    .group_segment_fixed_size: 73728
    .kernarg_segment_align: 8
    .kernarg_segment_size: 64
    .language:       OpenCL C
    .language_version:
      - 2
      - 0
    .max_flat_workgroup_size: 256
    .name:           _Z9attn_mfmaPKDF16_S0_S0_S0_S0_S0_PDF16_S1_
    .private_segment_fixed_size: 0
    .sgpr_count:     28
    .sgpr_spill_count: 0
    .symbol:         _Z9attn_mfmaPKDF16_S0_S0_S0_S0_S0_PDF16_S1_.kd
    .uniform_work_group_size: 1
    .uses_dynamic_stack: false
    .vgpr_count:     219
    .vgpr_spill_count: 0
    .wavefront_size: 64
  - .agpr_count:     0
    .args:
      - .actual_access:  read_only
        .address_space:  global
        .offset:         0
        .size:           8
        .value_kind:     global_buffer
      - .actual_access:  write_only
        .address_space:  global
        .offset:         8
        .size:           8
        .value_kind:     global_buffer
      - .actual_access:  read_only
        .address_space:  global
        .offset:         16
        .size:           8
        .value_kind:     global_buffer
      - .actual_access:  read_only
        .address_space:  global
        .offset:         24
        .size:           8
        .value_kind:     global_buffer
      - .actual_access:  read_only
        .address_space:  global
        .offset:         32
        .size:           8
        .value_kind:     global_buffer
      - .actual_access:  read_only
        .address_space:  global
        .offset:         40
        .size:           8
        .value_kind:     global_buffer
      - .actual_access:  read_only
        .address_space:  global
        .offset:         48
        .size:           8
        .value_kind:     global_buffer
      - .actual_access:  read_only
        .address_space:  global
        .offset:         56
        .size:           8
        .value_kind:     global_buffer
      - .actual_access:  write_only
        .address_space:  global
        .offset:         64
        .size:           8
        .value_kind:     global_buffer
      - .actual_access:  write_only
        .address_space:  global
        .offset:         72
        .size:           8
        .value_kind:     global_buffer
      - .actual_access:  read_only
        .address_space:  global
        .offset:         80
        .size:           8
        .value_kind:     global_buffer
      - .actual_access:  write_only
        .address_space:  global
        .offset:         88
        .size:           8
        .value_kind:     global_buffer
      - .actual_access:  write_only
        .address_space:  global
        .offset:         96
        .size:           8
        .value_kind:     global_buffer
      - .actual_access:  read_only
        .address_space:  global
        .offset:         104
        .size:           8
        .value_kind:     global_buffer
      - .actual_access:  write_only
        .address_space:  global
        .offset:         112
        .size:           8
        .value_kind:     global_buffer
      - .actual_access:  write_only
        .address_space:  global
        .offset:         120
        .size:           8
        .value_kind:     global_buffer
    .group_segment_fixed_size: 16640
    .kernarg_segment_align: 8
    .kernarg_segment_size: 128
    .language:       OpenCL C
    .language_version:
      - 2
      - 0
    .max_flat_workgroup_size: 256
    .name:           _Z14fused_ln_wprepILb0EEvPKfPfS1_S1_PKiS4_S1_S1_PDF16_S5_S1_S5_S5_S1_S5_S5_
    .private_segment_fixed_size: 0
    .sgpr_count:     24
    .sgpr_spill_count: 0
    .symbol:         _Z14fused_ln_wprepILb0EEvPKfPfS1_S1_PKiS4_S1_S1_PDF16_S5_S1_S5_S5_S1_S5_S5_.kd
    .uniform_work_group_size: 1
    .uses_dynamic_stack: false
    .vgpr_count:     44
    .vgpr_spill_count: 0
    .wavefront_size: 64
  - .agpr_count:     0
    .args:
      - .actual_access:  read_only
        .address_space:  global
        .offset:         0
        .size:           8
        .value_kind:     global_buffer
      - .actual_access:  write_only
        .address_space:  global
        .offset:         8
        .size:           8
        .value_kind:     global_buffer
      - .actual_access:  read_only
        .address_space:  global
        .offset:         16
        .size:           8
        .value_kind:     global_buffer
      - .actual_access:  read_only
        .address_space:  global
        .offset:         24
        .size:           8
        .value_kind:     global_buffer
      - .actual_access:  read_only
        .address_space:  global
        .offset:         32
        .size:           8
        .value_kind:     global_buffer
      - .actual_access:  read_only
        .address_space:  global
        .offset:         40
        .size:           8
        .value_kind:     global_buffer
      - .actual_access:  read_only
        .address_space:  global
        .offset:         48
        .size:           8
        .value_kind:     global_buffer
      - .actual_access:  read_only
        .address_space:  global
        .offset:         56
        .size:           8
        .value_kind:     global_buffer
      - .actual_access:  write_only
        .address_space:  global
        .offset:         64
        .size:           8
        .value_kind:     global_buffer
      - .actual_access:  write_only
        .address_space:  global
        .offset:         72
        .size:           8
        .value_kind:     global_buffer
      - .actual_access:  read_only
        .address_space:  global
        .offset:         80
        .size:           8
        .value_kind:     global_buffer
      - .actual_access:  write_only
        .address_space:  global
        .offset:         88
        .size:           8
        .value_kind:     global_buffer
      - .actual_access:  write_only
        .address_space:  global
        .offset:         96
        .size:           8
        .value_kind:     global_buffer
      - .actual_access:  read_only
        .address_space:  global
        .offset:         104
        .size:           8
        .value_kind:     global_buffer
      - .actual_access:  write_only
        .address_space:  global
        .offset:         112
        .size:           8
        .value_kind:     global_buffer
      - .actual_access:  write_only
        .address_space:  global
        .offset:         120
        .size:           8
        .value_kind:     global_buffer
    .group_segment_fixed_size: 16640
    .kernarg_segment_align: 8
    .kernarg_segment_size: 128
    .language:       OpenCL C
    .language_version:
      - 2
      - 0
    .max_flat_workgroup_size: 256
    .name:           _Z14fused_ln_wprepILb1EEvPKfPfS1_S1_PKiS4_S1_S1_PDF16_S5_S1_S5_S5_S1_S5_S5_
    .private_segment_fixed_size: 0
    .sgpr_count:     26
    .sgpr_spill_count: 0
    .symbol:         _Z14fused_ln_wprepILb1EEvPKfPfS1_S1_PKiS4_S1_S1_PDF16_S5_S1_S5_S5_S1_S5_S5_.kd
    .uniform_work_group_size: 1
    .uses_dynamic_stack: false
    .vgpr_count:     47
    .vgpr_spill_count: 0
    .wavefront_size: 64
  - .agpr_count:     0
    .args:
      - .offset:         0
        .size:           184
        .value_kind:     by_value
      - .offset:         184
        .size:           4
        .value_kind:     hidden_block_count_x
      - .offset:         188
        .size:           4
        .value_kind:     hidden_block_count_y
      - .offset:         192
        .size:           4
        .value_kind:     hidden_block_count_z
      - .offset:         196
        .size:           2
        .value_kind:     hidden_group_size_x
      - .offset:         198
        .size:           2
        .value_kind:     hidden_group_size_y
      - .offset:         200
        .size:           2
        .value_kind:     hidden_group_size_z
      - .offset:         202
        .size:           2
        .value_kind:     hidden_remainder_x
      - .offset:         204
        .size:           2
        .value_kind:     hidden_remainder_y
      - .offset:         206
        .size:           2
        .value_kind:     hidden_remainder_z
      - .offset:         224
        .size:           8
        .value_kind:     hidden_global_offset_x
      - .offset:         232
        .size:           8
        .value_kind:     hidden_global_offset_y
      - .offset:         240
        .size:           8
        .value_kind:     hidden_global_offset_z
      - .offset:         248
        .size:           2
        .value_kind:     hidden_grid_dims
    .group_segment_fixed_size: 65536
    .kernarg_segment_align: 8
    .kernarg_segment_size: 440
    .language:       OpenCL C
    .language_version:
      - 2
      - 0
    .max_flat_workgroup_size: 256
    .name:           _Z12gemm2_kernelILi3ELi0ELb0ELi4ELi4EEv2GP
    .private_segment_fixed_size: 0
    .sgpr_count:     36
    .sgpr_spill_count: 0
    .symbol:         _Z12gemm2_kernelILi3ELi0ELb0ELi4ELi4EEv2GP.kd
    .uniform_work_group_size: 1
    .uses_dynamic_stack: false
    .vgpr_count:     158
    .vgpr_spill_count: 0
    .wavefront_size: 64
  - .agpr_count:     0
    .args:
      - .offset:         0
        .size:           184
        .value_kind:     by_value
      - .offset:         184
        .size:           4
        .value_kind:     hidden_block_count_x
      - .offset:         188
        .size:           4
        .value_kind:     hidden_block_count_y
      - .offset:         192
        .size:           4
        .value_kind:     hidden_block_count_z
      - .offset:         196
        .size:           2
        .value_kind:     hidden_group_size_x
      - .offset:         198
        .size:           2
        .value_kind:     hidden_group_size_y
      - .offset:         200
        .size:           2
        .value_kind:     hidden_group_size_z
      - .offset:         202
        .size:           2
        .value_kind:     hidden_remainder_x
      - .offset:         204
        .size:           2
        .value_kind:     hidden_remainder_y
      - .offset:         206
        .size:           2
        .value_kind:     hidden_remainder_z
      - .offset:         224
        .size:           8
        .value_kind:     hidden_global_offset_x
      - .offset:         232
        .size:           8
        .value_kind:     hidden_global_offset_y
      - .offset:         240
        .size:           8
        .value_kind:     hidden_global_offset_z
      - .offset:         248
        .size:           2
        .value_kind:     hidden_grid_dims
    .group_segment_fixed_size: 131072
    .kernarg_segment_align: 8
    .kernarg_segment_size: 440
    .language:       OpenCL C
    .language_version:
      - 2
      - 0
    .max_flat_workgroup_size: 256
    .name:           _Z13gemm64_kernelILi3ELi1ELb0ELi1EEv2GP
    .private_segment_fixed_size: 0
    .sgpr_count:     28
    .sgpr_spill_count: 0
    .symbol:         _Z13gemm64_kernelILi3ELi1ELb0ELi1EEv2GP.kd
    .uniform_work_group_size: 1
    .uses_dynamic_stack: false
    .vgpr_count:     222
    .vgpr_spill_count: 0
    .wavefront_size: 64
  - .agpr_count:     0
    .args:
      - .actual_access:  read_only
        .address_space:  global
        .offset:         0
        .size:           8
        .value_kind:     global_buffer
      - .actual_access:  read_only
        .address_space:  global
        .offset:         8
        .size:           8
        .value_kind:     global_buffer
      - .actual_access:  read_only
        .address_space:  global
        .offset:         16
        .size:           8
        .value_kind:     global_buffer
      - .actual_access:  read_only
        .address_space:  global
        .offset:         24
        .size:           8
        .value_kind:     global_buffer
      - .actual_access:  write_only
        .address_space:  global
        .offset:         32
        .size:           8
        .value_kind:     global_buffer
      - .actual_access:  write_only
        .address_space:  global
        .offset:         40
        .size:           8
        .value_kind:     global_buffer
      - .address_space:  global
        .offset:         48
        .size:           8
        .value_kind:     global_buffer
      - .actual_access:  write_only
        .address_space:  global
        .offset:         56
        .size:           8
        .value_kind:     global_buffer
      - .actual_access:  write_only
        .address_space:  global
        .offset:         64
        .size:           8
        .value_kind:     global_buffer
      - .actual_access:  write_only
        .address_space:  global
        .offset:         72
        .size:           8
        .value_kind:     global_buffer
      - .actual_access:  write_only
        .address_space:  global
        .offset:         80
        .size:           8
        .value_kind:     global_buffer
      - .actual_access:  read_only
        .address_space:  global
        .offset:         88
        .size:           8
        .value_kind:     global_buffer
      - .actual_access:  write_only
        .address_space:  global
        .offset:         96
        .size:           8
        .value_kind:     global_buffer
      - .actual_access:  write_only
        .address_space:  global
        .offset:         104
        .size:           8
        .value_kind:     global_buffer
      - .actual_access:  read_only
        .address_space:  global
        .offset:         112
        .size:           8
        .value_kind:     global_buffer
      - .actual_access:  write_only
        .address_space:  global
        .offset:         120
        .size:           8
        .value_kind:     global_buffer
    .group_segment_fixed_size: 34432
    .kernarg_segment_align: 8
    .kernarg_segment_size: 128
    .language:       OpenCL C
    .language_version:
      - 2
      - 0
    .max_flat_workgroup_size: 256
    .name:           _Z18fused_router_wprepILb1EEvPKfS1_S1_PKiPfS4_PiS5_S5_S5_S4_S1_PDF16_S6_S1_S6_
    .private_segment_fixed_size: 0
    .sgpr_count:     35
    .sgpr_spill_count: 0
    .symbol:         _Z18fused_router_wprepILb1EEvPKfS1_S1_PKiPfS4_PiS5_S5_S5_S4_S1_PDF16_S6_S1_S6_.kd
    .uniform_work_group_size: 1
    .uses_dynamic_stack: false
    .vgpr_count:     104
    .vgpr_spill_count: 0
    .wavefront_size: 64
  - .agpr_count:     0
    .args:
      - .actual_access:  read_only
        .address_space:  global
        .offset:         0
        .size:           8
        .value_kind:     global_buffer
      - .actual_access:  read_only
        .address_space:  global
        .offset:         8
        .size:           8
        .value_kind:     global_buffer
      - .actual_access:  read_only
        .address_space:  global
        .offset:         16
        .size:           8
        .value_kind:     global_buffer
      - .actual_access:  read_only
        .address_space:  global
        .offset:         24
        .size:           8
        .value_kind:     global_buffer
      - .actual_access:  write_only
        .address_space:  global
        .offset:         32
        .size:           8
        .value_kind:     global_buffer
      - .actual_access:  write_only
        .address_space:  global
        .offset:         40
        .size:           8
        .value_kind:     global_buffer
      - .address_space:  global
        .offset:         48
        .size:           8
        .value_kind:     global_buffer
      - .actual_access:  write_only
        .address_space:  global
        .offset:         56
        .size:           8
        .value_kind:     global_buffer
      - .actual_access:  write_only
        .address_space:  global
        .offset:         64
        .size:           8
        .value_kind:     global_buffer
      - .actual_access:  write_only
        .address_space:  global
        .offset:         72
        .size:           8
        .value_kind:     global_buffer
      - .actual_access:  write_only
        .address_space:  global
        .offset:         80
        .size:           8
        .value_kind:     global_buffer
      - .actual_access:  read_only
        .address_space:  global
        .offset:         88
        .size:           8
        .value_kind:     global_buffer
      - .actual_access:  write_only
        .address_space:  global
        .offset:         96
        .size:           8
        .value_kind:     global_buffer
      - .actual_access:  read_only
        .address_space:  global
        .offset:         104
        .size:           8
        .value_kind:     global_buffer
      - .actual_access:  read_only
        .address_space:  global
        .offset:         112
        .size:           8
        .value_kind:     global_buffer
      - .actual_access:  write_only
        .address_space:  global
        .offset:         120
        .size:           8
        .value_kind:     global_buffer
    .group_segment_fixed_size: 17792
    .kernarg_segment_align: 8
    .kernarg_segment_size: 128
    .language:       OpenCL C
    .language_version:
      - 2
      - 0
    .max_flat_workgroup_size: 256
    .name:           _Z18fused_router_wprepILb0EEvPKfS1_S1_PKiPfS4_PiS5_S5_S5_S4_S1_PDF16_S6_S1_S6_
    .private_segment_fixed_size: 0
    .sgpr_count:     35
    .sgpr_spill_count: 0
    .symbol:         _Z18fused_router_wprepILb0EEvPKfS1_S1_PKiPfS4_PiS5_S5_S5_S4_S1_PDF16_S6_S1_S6_.kd
    .uniform_work_group_size: 1
    .uses_dynamic_stack: false
    .vgpr_count:     99
    .vgpr_spill_count: 0
    .wavefront_size: 64
  - .agpr_count:     0
    .args:
      - .offset:         0
        .size:           184
        .value_kind:     by_value
      - .offset:         184
        .size:           4
        .value_kind:     hidden_block_count_x
      - .offset:         188
        .size:           4
        .value_kind:     hidden_block_count_y
      - .offset:         192
        .size:           4
        .value_kind:     hidden_block_count_z
      - .offset:         196
        .size:           2
        .value_kind:     hidden_group_size_x
      - .offset:         198
        .size:           2
        .value_kind:     hidden_group_size_y
      - .offset:         200
        .size:           2
        .value_kind:     hidden_group_size_z
      - .offset:         202
        .size:           2
        .value_kind:     hidden_remainder_x
      - .offset:         204
        .size:           2
        .value_kind:     hidden_remainder_y
      - .offset:         206
        .size:           2
        .value_kind:     hidden_remainder_z
      - .offset:         224
        .size:           8
        .value_kind:     hidden_global_offset_x
      - .offset:         232
        .size:           8
        .value_kind:     hidden_global_offset_y
      - .offset:         240
        .size:           8
        .value_kind:     hidden_global_offset_z
      - .offset:         248
        .size:           2
        .value_kind:     hidden_grid_dims
    .group_segment_fixed_size: 65536
    .kernarg_segment_align: 8
    .kernarg_segment_size: 440
    .language:       OpenCL C
    .language_version:
      - 2
      - 0
    .max_flat_workgroup_size: 256
    .name:           _Z13gemm64_kernelILi3ELi2ELb1ELi1EEv2GP
    .private_segment_fixed_size: 0
    .sgpr_count:     42
    .sgpr_spill_count: 0
    .symbol:         _Z13gemm64_kernelILi3ELi2ELb1ELi1EEv2GP.kd
    .uniform_work_group_size: 1
    .uses_dynamic_stack: false
    .vgpr_count:     222
    .vgpr_spill_count: 0
    .wavefront_size: 64
  - .agpr_count:     0
    .args:
      - .offset:         0
        .size:           184
        .value_kind:     by_value
      - .offset:         184
        .size:           4
        .value_kind:     hidden_block_count_x
      - .offset:         188
        .size:           4
        .value_kind:     hidden_block_count_y
      - .offset:         192
        .size:           4
        .value_kind:     hidden_block_count_z
      - .offset:         196
        .size:           2
        .value_kind:     hidden_group_size_x
      - .offset:         198
        .size:           2
        .value_kind:     hidden_group_size_y
      - .offset:         200
        .size:           2
        .value_kind:     hidden_group_size_z
      - .offset:         202
        .size:           2
        .value_kind:     hidden_remainder_x
      - .offset:         204
        .size:           2
        .value_kind:     hidden_remainder_y
      - .offset:         206
        .size:           2
        .value_kind:     hidden_remainder_z
      - .offset:         224
        .size:           8
        .value_kind:     hidden_global_offset_x
      - .offset:         232
        .size:           8
        .value_kind:     hidden_global_offset_y
      - .offset:         240
        .size:           8
        .value_kind:     hidden_global_offset_z
      - .offset:         248
        .size:           2
        .value_kind:     hidden_grid_dims
    .group_segment_fixed_size: 32768
    .kernarg_segment_align: 8
    .kernarg_segment_size: 440
    .language:       OpenCL C
    .language_version:
      - 2
      - 0
    .max_flat_workgroup_size: 256
    .name:           _Z13gemm64_kernelILi1ELi2ELb1ELi1EEv2GP
    .private_segment_fixed_size: 0
    .sgpr_count:     34
    .sgpr_spill_count: 0
    .symbol:         _Z13gemm64_kernelILi1ELi2ELb1ELi1EEv2GP.kd
    .uniform_work_group_size: 1
    .uses_dynamic_stack: false
    .vgpr_count:     146
    .vgpr_spill_count: 0
    .wavefront_size: 64
  - .agpr_count:     0
    .args:
      - .actual_access:  read_only
        .address_space:  global
        .offset:         0
        .size:           8
        .value_kind:     global_buffer
      - .actual_access:  write_only
        .address_space:  global
        .offset:         8
        .size:           8
        .value_kind:     global_buffer
      - .actual_access:  write_only
        .address_space:  global
        .offset:         16
        .size:           8
        .value_kind:     global_buffer
      - .offset:         24
        .size:           4
        .value_kind:     by_value
      - .offset:         28
        .size:           4
        .value_kind:     by_value
    .group_segment_fixed_size: 16640
    .kernarg_segment_align: 8
    .kernarg_segment_size: 32
    .language:       OpenCL C
    .language_version:
      - 2
      - 0
    .max_flat_workgroup_size: 256
    .name:           _Z12wprep_kernelILb1EEvPKfPDF16_S2_ii
    .private_segment_fixed_size: 0
    .sgpr_count:     23
    .sgpr_spill_count: 0
    .symbol:         _Z12wprep_kernelILb1EEvPKfPDF16_S2_ii.kd
    .uniform_work_group_size: 1
    .uses_dynamic_stack: false
    .vgpr_count:     38
    .vgpr_spill_count: 0
    .wavefront_size: 64
  - .agpr_count:     0
    .args:
      - .offset:         0
        .size:           184
        .value_kind:     by_value
      - .offset:         184
        .size:           4
        .value_kind:     hidden_block_count_x
      - .offset:         188
        .size:           4
        .value_kind:     hidden_block_count_y
      - .offset:         192
        .size:           4
        .value_kind:     hidden_block_count_z
      - .offset:         196
        .size:           2
        .value_kind:     hidden_group_size_x
      - .offset:         198
        .size:           2
        .value_kind:     hidden_group_size_y
      - .offset:         200
        .size:           2
        .value_kind:     hidden_group_size_z
      - .offset:         202
        .size:           2
        .value_kind:     hidden_remainder_x
      - .offset:         204
        .size:           2
        .value_kind:     hidden_remainder_y
      - .offset:         206
        .size:           2
        .value_kind:     hidden_remainder_z
      - .offset:         224
        .size:           8
        .value_kind:     hidden_global_offset_x
      - .offset:         232
        .size:           8
        .value_kind:     hidden_global_offset_y
      - .offset:         240
        .size:           8
        .value_kind:     hidden_global_offset_z
      - .offset:         248
        .size:           2
        .value_kind:     hidden_grid_dims
    .group_segment_fixed_size: 65536
    .kernarg_segment_align: 8
    .kernarg_segment_size: 440
    .language:       OpenCL C
    .language_version:
      - 2
      - 0
    .max_flat_workgroup_size: 256
    .name:           _Z13gemm64_kernelILi3ELi3ELb1ELi2EEv2GP
    .private_segment_fixed_size: 0
    .sgpr_count:     44
    .sgpr_spill_count: 0
    .symbol:         _Z13gemm64_kernelILi3ELi3ELb1ELi2EEv2GP.kd
    .uniform_work_group_size: 1
    .uses_dynamic_stack: false
    .vgpr_count:     222
    .vgpr_spill_count: 0
    .wavefront_size: 64
  - .agpr_count:     0
    .args:
      - .offset:         0
        .size:           184
        .value_kind:     by_value
      - .offset:         184
        .size:           4
        .value_kind:     hidden_block_count_x
      - .offset:         188
        .size:           4
        .value_kind:     hidden_block_count_y
      - .offset:         192
        .size:           4
        .value_kind:     hidden_block_count_z
      - .offset:         196
        .size:           2
        .value_kind:     hidden_group_size_x
      - .offset:         198
        .size:           2
        .value_kind:     hidden_group_size_y
      - .offset:         200
        .size:           2
        .value_kind:     hidden_group_size_z
      - .offset:         202
        .size:           2
        .value_kind:     hidden_remainder_x
      - .offset:         204
        .size:           2
        .value_kind:     hidden_remainder_y
      - .offset:         206
        .size:           2
        .value_kind:     hidden_remainder_z
      - .offset:         224
        .size:           8
        .value_kind:     hidden_global_offset_x
      - .offset:         232
        .size:           8
        .value_kind:     hidden_global_offset_y
      - .offset:         240
        .size:           8
        .value_kind:     hidden_global_offset_z
      - .offset:         248
        .size:           2
        .value_kind:     hidden_grid_dims
    .group_segment_fixed_size: 32768
    .kernarg_segment_align: 8
    .kernarg_segment_size: 440
    .language:       OpenCL C
    .language_version:
      - 2
      - 0
    .max_flat_workgroup_size: 256
    .name:           _Z13gemm64_kernelILi1ELi3ELb1ELi1EEv2GP
    .private_segment_fixed_size: 0
    .sgpr_count:     34
    .sgpr_spill_count: 0
    .symbol:         _Z13gemm64_kernelILi1ELi3ELb1ELi1EEv2GP.kd
    .uniform_work_group_size: 1
    .uses_dynamic_stack: false
    .vgpr_count:     118
    .vgpr_spill_count: 0
    .wavefront_size: 64
  - .agpr_count:     0
    .args:
      - .actual_access:  read_only
        .address_space:  global
        .offset:         0
        .size:           8
        .value_kind:     global_buffer
      - .actual_access:  write_only
        .address_space:  global
        .offset:         8
        .size:           8
        .value_kind:     global_buffer
      - .actual_access:  read_only
        .address_space:  global
        .offset:         16
        .size:           8
        .value_kind:     global_buffer
      - .actual_access:  read_only
        .address_space:  global
        .offset:         24
        .size:           8
        .value_kind:     global_buffer
      - .actual_access:  read_only
        .address_space:  global
        .offset:         32
        .size:           8
        .value_kind:     global_buffer
      - .actual_access:  read_only
        .address_space:  global
        .offset:         40
        .size:           8
        .value_kind:     global_buffer
      - .actual_access:  read_only
        .address_space:  global
        .offset:         48
        .size:           8
        .value_kind:     global_buffer
      - .actual_access:  read_only
        .address_space:  global
        .offset:         56
        .size:           8
        .value_kind:     global_buffer
      - .actual_access:  read_only
        .address_space:  global
        .offset:         64
        .size:           8
        .value_kind:     global_buffer
      - .actual_access:  read_only
        .address_space:  global
        .offset:         72
        .size:           8
        .value_kind:     global_buffer
    .group_segment_fixed_size: 0
    .kernarg_segment_align: 8
    .kernarg_segment_size: 80
    .language:       OpenCL C
    .language_version:
      - 2
      - 0
    .max_flat_workgroup_size: 256
    .name:           _Z17combine_ln_kernelILb1ELb0EEvPKfPfS1_S1_PKiS4_S1_S1_PDF16_S5_
    .private_segment_fixed_size: 0
    .sgpr_count:     22
    .sgpr_spill_count: 0
    .symbol:         _Z17combine_ln_kernelILb1ELb0EEvPKfPfS1_S1_PKiS4_S1_S1_PDF16_S5_.kd
    .uniform_work_group_size: 1
    .uses_dynamic_stack: false
    .vgpr_count:     32
    .vgpr_spill_count: 0
    .wavefront_size: 64
